# rider split 4 tiles in the GQA units / 20 in the differential units
# speedup vs baseline: 1.0288x; 1.0133x over previous
; DI f32x16 mfma8(v8i a, v8i b, f32x16 c) { return __builtin_amdgcn_mfma_scale_f32_32x32x64_f8f6f4(a, b, c, 0, 0, 0, 0, 0, 0); }
; DI void attn_unit_d8(unsigned char* lds, const AttnArgs& a) {
;     ...
;     auto tile = [&](const unsigned char* Kb, const unsigned char* Kn, v8i& Pa, v8i& Pb, v8i& v0, v8i& v1, const v8i& Qa, const v8i& Qb, const v8i& w0, const v8i& w1) __attribute__((always_inline)) {
;         qk(Kb, 1, s1a, s1b);
;         v0 = rd32(Kb + voff); v1 = rd32(Kb + voff + 32 * A8_PITCH);
;         o0[0] = mfma8(w0, Qa, o0[0]); o1[0] = mfma8(w0, Qb, o1[0]); o0[1] = mfma8(w1, Qa, o0[1]); o1[1] = mfma8(w1, Qb, o1[1]);
;         expsum(s0a, l0); expsum(s0b, l1); pack4(s0a, Pa, 0); pack4(s0b, Pb, 0);
;         qk(Kn, 0, s0a, s0b);
;         expsum(s1a, l0); expsum(s1b, l1); pack4(s1a, Pa, 4); pack4(s1b, Pb, 4);
; #pragma unroll
;         for (int i = 0; i < 8; ++i) { __builtin_amdgcn_sched_group_barrier(0x008, 1, 0); __builtin_amdgcn_sched_group_barrier(0x402, 22, 0); }
;     };
;     for (int t = a.t0; t < a.t1; t += 2) {
;         const int s1 = sb + 1 >= 5 ? sb - 4 : sb + 1, s2 = sb + 2 >= 5 ? sb - 3 : sb + 2, s3 = sb + 3 >= 5 ? sb - 2 : sb + 3, s4 = sb + 4 >= 5 ? sb - 1 : sb + 4;
;         { const int ta = t + 3, tb = t + 4; gload(ta < a.t1 ? ta : a.t1 - 1, kreg0, vreg0); gload(tb < a.t1 ? tb : a.t1 - 1, kreg1, vreg1); }
;         tile(lds + sb * D8_SLOT, lds + s1 * D8_SLOT, PaX, PbX, vX0, vX1, PaY, PbY, vY0, vY1);
;         tile(lds + s1 * D8_SLOT, lds + s2 * D8_SLOT, PaY, PbY, vY0, vY1, PaX, PbX, vX0, vX1);
.LBB0_663:
	s_cmp_gt_i32 s16, 3
	s_cselect_b32 s17, -4, 1
	s_add_i32 s18, s17, s16
	s_mul_i32 s6, s16, 0x2800
	s_cmp_gt_i32 s16, 2
	v_mfma_f32_32x32x64_f8f6f4 v[50:65], v[154:161], v[138:145], v[50:65]
	v_exp_f32_e32 v192, v90
	v_add_u32_e32 v90, s6, v218
	s_cselect_b32 s6, -3, 2
	s_add_i32 s6, s6, s16
	s_cmp_gt_i32 s16, 1
	s_cselect_b32 s19, -2, 3
	s_add_i32 s19, s19, s16
	s_cmp_gt_i32 s16, 0
	s_cselect_b32 s49, -1, 4
	s_min_u32 s54, s46, 64
	s_add_i32 s49, s49, s16
	s_cmp_lt_u32 s46, 61
	s_mul_i32 s17, s6, 0x2800
	s_mov_b32 s16, s6
	s_cselect_b64 s[52:53], -1, 0
	s_lshl_b32 s6, s54, 6
	s_add_i32 s54, s6, 0xc0
	s_add_i32 s55, s6, 0xfffff0c0
	s_and_b64 s[52:53], s[52:53], exec
	v_lshl_add_u64 v[98:99], v[182:183], 0, s[6:7]
	s_cselect_b32 s6, s54, s55
	s_cselect_b32 s53, s21, s48
	s_cselect_b32 s52, s20, s47
	s_min_u32 s56, s46, 63
	v_exp_f32_e32 v198, v82
	v_exp_f32_e32 v199, v83
	v_exp_f32_e32 v196, v84
	v_exp_f32_e32 v197, v85
	v_exp_f32_e32 v200, v86
	v_exp_f32_e32 v201, v87
	v_exp_f32_e32 v194, v88
	v_exp_f32_e32 v195, v89
	ds_read_b128 v[82:85], v90 offset:2560
	ds_read_b128 v[86:89], v90 offset:2576
	global_load_dwordx2 v[202:203], v[98:99], off offset:192
	v_add_u32_e32 v98, s6, v215
	s_cmp_lt_u32 s46, 60
	v_ashrrev_i32_e32 v99, 31, v98
	s_cselect_b64 s[54:55], -1, 0
	s_lshl_b32 s6, s56, 6
	v_lshlrev_b64 v[98:99], 8, v[98:99]
	s_add_i32 s56, s6, 0x100
	s_add_i32 s57, s6, 0xfffff100
	v_lshl_add_u64 v[98:99], s[52:53], 0, v[98:99]
	s_and_b64 s[52:53], s[54:55], exec
	s_cselect_b32 s54, s56, s57
	v_lshl_add_u64 v[220:221], v[98:99], 0, v[178:179]
	v_add_u32_e32 v98, s54, v215
	v_ashrrev_i32_e32 v99, 31, v98
	s_cselect_b32 s53, s21, s48
	s_cselect_b32 s52, s20, s47
	v_lshlrev_b64 v[98:99], 8, v[98:99]
	v_lshl_add_u64 v[100:101], v[182:183], 0, s[6:7]
	v_lshl_add_u64 v[98:99], s[52:53], 0, v[98:99]
	global_load_dwordx2 v[204:205], v[100:101], off offset:256
	v_lshl_add_u64 v[222:223], v[98:99], 0, v[178:179]
	s_waitcnt lgkmcnt(0)
	v_mfma_f32_32x32x64_f8f6f4 v[98:113], v[82:89], v[114:121], 0
	v_exp_f32_e32 v193, v91
	v_exp_f32_e32 v224, v92
	v_exp_f32_e32 v225, v93
	v_exp_f32_e32 v226, v94
	v_exp_f32_e32 v227, v95
	v_exp_f32_e32 v228, v96
	v_exp_f32_e32 v229, v97
	ds_read_b128 v[170:173], v90 offset:5120
	ds_read_b128 v[174:177], v90 offset:5136
	ds_read_b128 v[162:165], v90 offset:7680
	ds_read_b128 v[166:169], v90 offset:7696
	v_pk_add_f32 v[90:91], v[186:187], v[198:199]
	v_pk_add_f32 v[92:93], v[184:185], v[196:197]
	v_pk_add_f32 v[90:91], v[200:201], v[90:91]
	v_pk_add_f32 v[92:93], v[194:195], v[92:93]
	v_pk_add_f32 v[90:91], v[192:193], v[90:91]
	v_pk_add_f32 v[92:93], v[224:225], v[92:93]
	v_exp_f32_e32 v66, v66
	v_exp_f32_e32 v67, v67
	v_exp_f32_e32 v68, v68
	v_exp_f32_e32 v69, v69
	v_exp_f32_e32 v70, v70
	v_exp_f32_e32 v71, v71
	v_exp_f32_e32 v72, v72
	v_pk_add_f32 v[230:231], v[228:229], v[92:93]
	v_pk_add_f32 v[232:233], v[226:227], v[90:91]
	v_mfma_f32_32x32x64_f8f6f4 v[82:97], v[82:89], v[122:129], 0
	v_exp_f32_e32 v73, v73
	v_exp_f32_e32 v74, v74
	v_exp_f32_e32 v75, v75
	v_exp_f32_e32 v76, v76
	v_exp_f32_e32 v77, v77
	v_exp_f32_e32 v78, v78
	v_exp_f32_e32 v79, v79
	v_exp_f32_e32 v80, v80
	v_exp_f32_e32 v81, v81
	v_pk_add_f32 v[186:187], v[190:191], v[66:67]
	v_pk_add_f32 v[188:189], v[188:189], v[68:69]
	s_nop 0
	v_pk_add_f32 v[186:187], v[70:71], v[186:187]
	v_pk_add_f32 v[188:189], v[72:73], v[188:189]
	s_nop 0
	v_cvt_scalef32_pk_fp8_f32 v184, v198, v199, s36
	v_pk_add_f32 v[186:187], v[74:75], v[186:187]
	v_pk_add_f32 v[188:189], v[76:77], v[188:189]
	v_cvt_scalef32_pk_fp8_f32 v185, v200, v201, s36
	v_cvt_scalef32_pk_fp8_f32 v184, v196, v197, s36 op_sel:[0,0,0,1]
	v_pk_add_f32 v[190:191], v[78:79], v[186:187]
	v_pk_add_f32 v[188:189], v[80:81], v[188:189]
	v_mfma_f32_32x32x64_f8f6f4 v[2:17], v[154:161], v[130:137], v[2:17]
	s_nop 0
	s_nop 0
	s_nop 0
	s_nop 0
	s_nop 0
	s_nop 0
	s_mulk_i32 s18, 0x2800
	v_cvt_scalef32_pk_fp8_f32 v186, v192, v193, s36
	v_cvt_scalef32_pk_fp8_f32 v187, v226, v227, s36
	v_cvt_scalef32_pk_fp8_f32 v154, v66, v67, s36
	v_cvt_scalef32_pk_fp8_f32 v155, v70, v71, s36
	v_cvt_scalef32_pk_fp8_f32 v156, v74, v75, s36
	v_cvt_scalef32_pk_fp8_f32 v157, v78, v79, s36
	v_cvt_scalef32_pk_fp8_f32 v185, v194, v195, s36 op_sel:[0,0,0,1]
	v_add_u32_e32 v219, s18, v218
	v_cvt_scalef32_pk_fp8_f32 v186, v224, v225, s36 op_sel:[0,0,0,1]
	v_cvt_scalef32_pk_fp8_f32 v187, v228, v229, s36 op_sel:[0,0,0,1]
	v_cvt_scalef32_pk_fp8_f32 v154, v68, v69, s36 op_sel:[0,0,0,1]
	v_cvt_scalef32_pk_fp8_f32 v155, v72, v73, s36 op_sel:[0,0,0,1]
	v_cvt_scalef32_pk_fp8_f32 v156, v76, v77, s36 op_sel:[0,0,0,1]
	v_cvt_scalef32_pk_fp8_f32 v157, v80, v81, s36 op_sel:[0,0,0,1]
	v_exp_f32_e32 v98, v98
	v_exp_f32_e32 v99, v99
	v_mfma_f32_32x32x64_f8f6f4 v[34:49], v[146:153], v[138:145], v[34:49]
	v_exp_f32_e32 v100, v100
	v_exp_f32_e32 v101, v101
	v_exp_f32_e32 v102, v102
	v_exp_f32_e32 v103, v103
	v_exp_f32_e32 v104, v104
	v_exp_f32_e32 v105, v105
	v_exp_f32_e32 v106, v106
	v_exp_f32_e32 v107, v107
	v_exp_f32_e32 v108, v108
	v_exp_f32_e32 v109, v109
	v_exp_f32_e32 v110, v110
	v_exp_f32_e32 v111, v111
	v_exp_f32_e32 v112, v112
	v_exp_f32_e32 v113, v113
	ds_read_b128 v[192:195], v219
	ds_read_b128 v[196:199], v219 offset:16
	v_pk_add_f32 v[66:67], v[232:233], v[98:99]
	v_pk_add_f32 v[68:69], v[230:231], v[100:101]
	v_pk_add_f32 v[66:67], v[102:103], v[66:67]
	v_pk_add_f32 v[68:69], v[104:105], v[68:69]
	v_pk_add_f32 v[66:67], v[106:107], v[66:67]
	v_pk_add_f32 v[68:69], v[108:109], v[68:69]
	v_pk_add_f32 v[140:141], v[110:111], v[66:67]
	v_pk_add_f32 v[138:139], v[112:113], v[68:69]
	v_mfma_f32_32x32x64_f8f6f4 v[18:33], v[146:153], v[130:137], v[18:33]
	v_exp_f32_e32 v82, v82
	v_exp_f32_e32 v83, v83
	v_exp_f32_e32 v84, v84
	v_exp_f32_e32 v85, v85
	v_exp_f32_e32 v86, v86
	v_exp_f32_e32 v87, v87
	v_exp_f32_e32 v88, v88
	v_exp_f32_e32 v89, v89
	v_exp_f32_e32 v90, v90
	v_exp_f32_e32 v91, v91
	v_exp_f32_e32 v92, v92
	v_exp_f32_e32 v93, v93
	v_exp_f32_e32 v94, v94
	v_exp_f32_e32 v95, v95
	v_exp_f32_e32 v96, v96
	v_exp_f32_e32 v97, v97
	v_pk_add_f32 v[66:67], v[190:191], v[82:83]
	v_pk_add_f32 v[68:69], v[188:189], v[84:85]
	v_pk_add_f32 v[66:67], v[86:87], v[66:67]
	v_pk_add_f32 v[68:69], v[88:89], v[68:69]
	v_pk_add_f32 v[130:131], v[90:91], v[66:67]
	v_pk_add_f32 v[132:133], v[92:93], v[68:69]
	s_waitcnt lgkmcnt(0)
; DI void attn_unit_a8(unsigned char* lds, const AttnArgs& a) {
;     ...
;     auto w_decode = [&](int j, const float*& src, unsigned char*& dst, int& ld, int& n0, int& k0, bool& gu) __attribute__((always_inline)) {
;         const int g = (j >> 2) * 512 + a.wl, e = g / 96, rr = g - e * 96; KParamsPtr kp = kparams();
;         if (rr < 64) { src = kp->w_gu + ((size_t)a.wli * NE + e) * (1024 * 2048); dst = kp->ws + WS_WGU + (size_t)a.wli * SZ_WGU + (size_t)e * 2048 * 1024; ld = 2048; n0 = (rr & 7) * 256; k0 = ((rr >> 3) * 4 + (j & 3)) * 32; gu = true; }
;         else { const int q = rr - 64; src = kp->w_dn + ((size_t)a.wli * NE + e) * (1024 * 1024); dst = kp->ws + WS_WDN + (size_t)a.wli * SZ_WDN + (size_t)e * 1024 * 1024; ld = 1024; n0 = (q & 3) * 256; k0 = ((q >> 2) * 4 + (j & 3)) * 32; gu = false; } };
;     auto w_issue = [&](int j) __attribute__((always_inline)) { const float* src; unsigned char* dst; int ld, n0, k0; bool gu; w_decode(j, src, dst, ld, n0, k0, gu);
;         const float* p = src + (size_t)(k0 + 4 * wid) * ld + n0 + wn4;
;         wq[0] = __builtin_nontemporal_load((const f32x4*)p); wq[1] = __builtin_nontemporal_load((const f32x4*)(p + ld));
; DI void attn_unit_d8(unsigned char* lds, const AttnArgs& a) {
;     ...
;     auto tile = [&](const unsigned char* Kb, const unsigned char* Kn, v8i& Pa, v8i& Pb, v8i& v0, v8i& v1, const v8i& Qa, const v8i& Qb, const v8i& w0, const v8i& w1) __attribute__((always_inline)) {
;         qk(Kb, 1, s1a, s1b);
;         v0 = rd32(Kb + voff); v1 = rd32(Kb + voff + 32 * A8_PITCH);
;         o0[0] = mfma8(w0, Qa, o0[0]); o1[0] = mfma8(w0, Qb, o1[0]); o0[1] = mfma8(w1, Qa, o0[1]); o1[1] = mfma8(w1, Qb, o1[1]);
;         expsum(s0a, l0); expsum(s0b, l1); pack4(s0a, Pa, 0); pack4(s0b, Pb, 0);
;         qk(Kn, 0, s0a, s0b);
;         expsum(s1a, l0); expsum(s1b, l1); pack4(s1a, Pa, 4); pack4(s1b, Pb, 4);
; #pragma unroll
;         for (int i = 0; i < 8; ++i) { __builtin_amdgcn_sched_group_barrier(0x008, 1, 0); __builtin_amdgcn_sched_group_barrier(0x402, 22, 0); }
;     };
;     for (int t = a.t0; t < a.t1; t += 2) {
;         const int s1 = sb + 1 >= 5 ? sb - 4 : sb + 1, s2 = sb + 2 >= 5 ? sb - 3 : sb + 2, s3 = sb + 3 >= 5 ? sb - 2 : sb + 3, s4 = sb + 4 >= 5 ? sb - 1 : sb + 4;
;         { const int ta = t + 3, tb = t + 4; gload(ta < a.t1 ? ta : a.t1 - 1, kreg0, vreg0); gload(tb < a.t1 ? tb : a.t1 - 1, kreg1, vreg1); }
	v_mfma_f32_32x32x64_f8f6f4 v[66:81], v[192:199], v[114:121], 0
	s_nop 0
	s_nop 0
	s_nop 0
	s_nop 0
	s_nop 0
	s_nop 0
	s_nop 0
	v_cvt_scalef32_pk_fp8_f32 v188, v98, v99, s36
	v_cvt_scalef32_pk_fp8_f32 v189, v102, v103, s36
	v_cvt_scalef32_pk_fp8_f32 v190, v106, v107, s36
	v_cvt_scalef32_pk_fp8_f32 v191, v110, v111, s36
	v_cvt_scalef32_pk_fp8_f32 v158, v82, v83, s36
	v_cvt_scalef32_pk_fp8_f32 v159, v86, v87, s36
	v_pk_add_f32 v[142:143], v[96:97], v[132:133]
	v_pk_add_f32 v[144:145], v[94:95], v[130:131]
	v_cvt_scalef32_pk_fp8_f32 v160, v90, v91, s36
	v_cvt_scalef32_pk_fp8_f32 v188, v100, v101, s36 op_sel:[0,0,0,1]
	v_cvt_scalef32_pk_fp8_f32 v189, v104, v105, s36 op_sel:[0,0,0,1]
	v_cvt_scalef32_pk_fp8_f32 v190, v108, v109, s36 op_sel:[0,0,0,1]
	v_cvt_scalef32_pk_fp8_f32 v191, v112, v113, s36 op_sel:[0,0,0,1]
	v_cvt_scalef32_pk_fp8_f32 v158, v84, v85, s36 op_sel:[0,0,0,1]
	v_cvt_scalef32_pk_fp8_f32 v159, v88, v89, s36 op_sel:[0,0,0,1]
	v_mfma_f32_32x32x64_f8f6f4 v[98:113], v[192:199], v[122:129], 0
	global_load_dwordx2 v[192:193], v[220:221], off
	global_load_dwordx2 v[194:195], v[222:223], off
	ds_read_b128 v[130:133], v219 offset:2560
	ds_read_b128 v[134:137], v219 offset:2576
	s_mulk_i32 s19, 0x2800
	s_nop 0
	v_exp_f32_e32 v146, v66
	s_lshr_b32 s73, s61, 2
	v_exp_f32_e32 v147, v67
	s_add_i32 s73, s73, 1
	v_exp_f32_e32 v148, v68
	s_lshl_b32 s73, s73, 9
	v_exp_f32_e32 v149, v69
	s_add_i32 s73, s73, s42
	s_add_i32 s19, s19, 0
	v_cvt_scalef32_pk_fp8_f32 v161, v94, v95, s36
	v_exp_f32_e32 v150, v70
	s_mul_i32 s75, s73, 0xaaab
	v_exp_f32_e32 v151, v71
	s_lshr_b32 s75, s75, 22
	v_exp_f32_e32 v152, v72
	s_mul_i32 s76, s75, 0x60
	v_exp_f32_e32 v153, v73
	s_sub_i32 s76, s73, s76
	v_add_u32_e32 v224, s19, v216
	v_add_u32_e32 v225, s19, v217
	v_cvt_scalef32_pk_fp8_f32 v160, v92, v93, s36 op_sel:[0,0,0,1]
	v_cvt_scalef32_pk_fp8_f32 v161, v96, v97, s36 op_sel:[0,0,0,1]
	v_exp_f32_e32 v196, v74
	s_lshr_b32 s77, s76, 6
	v_exp_f32_e32 v197, v75
	s_lshl_b32 s78, s77, 6
	v_exp_f32_e32 v198, v76
	s_sub_i32 s76, s76, s78
	v_exp_f32_e32 v199, v77
	s_sub_i32 s78, 3, s77
	v_exp_f32_e32 v200, v78
	s_lshr_b32 s79, s76, s78
	v_exp_f32_e32 v201, v79
	s_lshl_b32 s79, s79, 2
	v_exp_f32_e32 v220, v80
	s_and_b32 s81, s61, 3
	v_exp_f32_e32 v221, v81
	s_add_i32 s79, s79, s81
	s_waitcnt lgkmcnt(0)
	v_mfma_f32_32x32x64_f8f6f4 v[82:97], v[130:137], v[114:121], 0
	v_add_f32_e64 v66, v140, v146
	v_add_f32_e64 v67, v141, v147
	v_add_f32_e64 v68, v138, v148
	v_add_f32_e64 v69, v139, v149
	v_add_f32_e64 v66, v150, v66
	v_add_f32_e64 v67, v151, v67
	v_add_f32_e64 v68, v152, v68
	v_add_f32_e64 v69, v153, v69
	v_add_f32_e64 v138, v196, v66
	v_add_f32_e64 v139, v197, v67
	v_add_f32_e64 v140, v198, v68
	v_add_f32_e64 v141, v199, v69
	v_exp_f32_e32 v98, v98
	s_lshl_b32 s79, s79, 5
	v_exp_f32_e32 v99, v99
	s_lshl_b32 s81, s63, 2
	v_exp_f32_e32 v100, v100
	s_add_i32 s81, s81, s79
	v_exp_f32_e32 v101, v101
	s_sub_i32 s78, 13, s77
	v_exp_f32_e32 v102, v102
	s_lshl_b32 s81, s81, s78
	v_exp_f32_e32 v103, v103
	s_lshr_b32 s78, 7, s77
	v_exp_f32_e32 v104, v104
	s_and_b32 s78, s76, s78
	v_exp_f32_e32 v105, v105
	s_lshl_b32 s72, s78, 10
	v_exp_f32_e32 v106, v106
	s_add_i32 s81, s81, s72
	v_exp_f32_e32 v107, v107
	s_add_i32 s72, s75, 0
	v_exp_f32_e32 v108, v108
	s_sub_i32 s80, 23, s77
	v_exp_f32_e32 v109, v109
	s_lshl_b32 s72, s72, s80
	v_exp_f32_e32 v110, v110
	s_add_i32 s81, s81, s72
	v_exp_f32_e32 v111, v111
	s_cmp_eq_u32 s77, 0
	s_cselect_b64 s[84:85], s[66:67], s[68:69]
	v_exp_f32_e32 v112, v112
	s_add_u32 s84, s84, s81
	s_addc_u32 s85, s85, 0
	v_exp_f32_e32 v113, v113
	s_lshr_b32 s80, 0x2000, s77
	v_mfma_f32_32x32x64_f8f6f4 v[66:81], v[130:137], v[122:129], 0
	v_add_f32_e64 v130, v144, v98
	v_add_f32_e64 v131, v145, v99
	v_add_f32_e64 v132, v142, v100
	v_add_f32_e64 v133, v143, v101
	v_add_f32_e64 v142, v102, v130
	v_add_f32_e64 v143, v103, v131
	v_add_f32_e64 v132, v104, v132
	v_add_f32_e64 v133, v105, v133
	v_add_f32_e64 v134, v220, v140
	v_add_f32_e64 v135, v221, v141
	v_add_f32_e64 v136, v200, v138
	v_add_f32_e64 v137, v201, v139
	s_nop 0
	s_nop 0
	s_nop 0
	s_nop 0
	s_nop 0
	s_nop 0
	v_pk_add_f32 v[142:143], v[106:107], v[142:143]
	v_pk_add_f32 v[132:133], v[108:109], v[132:133]
	v_cvt_scalef32_pk_fp8_f32 v138, v146, v147, s36
	v_cvt_scalef32_pk_fp8_f32 v139, v150, v151, s36
	v_cvt_scalef32_pk_fp8_f32 v140, v196, v197, s36
	v_cvt_scalef32_pk_fp8_f32 v141, v200, v201, s36
	v_cvt_scalef32_pk_fp8_f32 v130, v98, v99, s36
	v_cvt_scalef32_pk_fp8_f32 v131, v102, v103, s36
	v_pk_add_f32 v[146:147], v[112:113], v[132:133]
	v_pk_add_f32 v[150:151], v[110:111], v[142:143]
	v_mfma_f32_32x32x64_f8f6f4 v[50:65], v[170:177], v[184:191], v[50:65]
	v_exp_f32_e32 v82, v82
	s_and_b32 s72, s78, 3
	v_exp_f32_e32 v83, v83
	s_lshl_b32 s72, s72, 19
	v_exp_f32_e32 v84, v84
	s_lshr_b32 s81, s78, 2
	v_exp_f32_e32 v85, v85
	s_lshl_b32 s81, s81, 17
	v_add_u32_e32 v102, s17, v218
	v_exp_f32_e32 v86, v86
	s_add_i32 s72, s72, s81
	v_exp_f32_e32 v87, v87
	s_lshl_b32 s81, s78, 18
	v_exp_f32_e32 v88, v88
	s_cmp_eq_u32 s77, 0
	s_cselect_b32 s72, s72, s81
; DI unsigned pk4_fp8_mul64(float a, float b, float c, float d) { v2s_t r = {0, 0}; r = __builtin_amdgcn_cvt_scalef32_pk_fp8_f32(r, a, b, 0.015625f, false); r = __builtin_amdgcn_cvt_scalef32_pk_fp8_f32(r, c, d, 0.015625f, true); return __builtin_bit_cast(unsigned, r); }
; DI f32x16 mfma8(v8i a, v8i b, f32x16 c) { return __builtin_amdgcn_mfma_scale_f32_32x32x64_f8f6f4(a, b, c, 0, 0, 0, 0, 0, 0); }
; DI void attn_unit_a8(unsigned char* lds, const AttnArgs& a) {
;     ...
;     auto w_cvt = [&]() __attribute__((always_inline)) { unsigned char* t8 = lds + AT_WT + wn4 * WPITCH + 4 * wid;
; #pragma unroll
;         for (int j = 0; j < 4; ++j) *(unsigned*)(t8 + j * WPITCH) = pk4_fp8_mul64(wq[0][j], wq[1][j], wq[2][j], wq[3][j]); };
;     const int wcol = tid >> 1, whalf = tid & 1;
;     const unsigned wper_gu = (unsigned)((wcol >> 7) * 256 + (wcol & 96) + invperm32(wcol & 31)) * 1024u + 16u * whalf;
;     const unsigned wper_dn = (unsigned)fwd_lane16(wcol) * 1024u + 16u * whalf;
;     auto w_store = [&](int j) __attribute__((always_inline)) { const float* src; unsigned char* dst; int ld, n0, k0; bool gu; w_decode(j, src, dst, ld, n0, k0, gu);
;         const int nb = n0 >> 8; const unsigned uni = (unsigned)(gu ? (nb & 3) * 512 + (nb >> 2) * 128 : nb * 256) * 1024u + (unsigned)k0;
;         const unsigned off = (gu ? wper_gu : wper_dn) + uni;
;         const unsigned* t = (const unsigned*)(lds + AT_WT + wcol * WPITCH + 16 * whalf);
;         *(u32x4*)(dst + off) = (u32x4){t[0], t[1], t[2], t[3]}; };
; DI void attn_unit_d8(unsigned char* lds, const AttnArgs& a) {
;     ...
;     auto tile = [&](const unsigned char* Kb, const unsigned char* Kn, v8i& Pa, v8i& Pb, v8i& v0, v8i& v1, const v8i& Qa, const v8i& Qb, const v8i& w0, const v8i& w1) __attribute__((always_inline)) {
;         qk(Kb, 1, s1a, s1b);
;         v0 = rd32(Kb + voff); v1 = rd32(Kb + voff + 32 * A8_PITCH);
;         o0[0] = mfma8(w0, Qa, o0[0]); o1[0] = mfma8(w0, Qb, o1[0]); o0[1] = mfma8(w1, Qa, o0[1]); o1[1] = mfma8(w1, Qb, o1[1]);
;         expsum(s0a, l0); expsum(s0b, l1); pack4(s0a, Pa, 0); pack4(s0b, Pb, 0);
;         qk(Kn, 0, s0a, s0b);
;         expsum(s1a, l0); expsum(s1b, l1); pack4(s1a, Pa, 4); pack4(s1b, Pb, 4);
; #pragma unroll
;         for (int i = 0; i < 8; ++i) { __builtin_amdgcn_sched_group_barrier(0x008, 1, 0); __builtin_amdgcn_sched_group_barrier(0x402, 22, 0); }
;     };
	v_exp_f32_e32 v89, v89
	s_mul_i32 s81, s77, 0x10000000
	v_cvt_scalef32_pk_fp8_f32 v130, v100, v101, s36 op_sel:[0,0,0,1]
	v_cvt_scalef32_pk_fp8_f32 v131, v104, v105, s36 op_sel:[0,0,0,1]
	v_exp_f32_e32 v90, v90
	s_add_i32 s81, s81, 0x1094000
	v_exp_f32_e32 v91, v91
	s_add_i32 s72, s72, s79
	v_exp_f32_e32 v92, v92
	s_sub_i32 s73, 21, s77
	v_exp_f32_e32 v93, v93
	s_lshl_b32 s73, s75, s73
	ds_read_b128 v[98:101], v102
	ds_read_b128 v[102:105], v102 offset:16
	s_nop 0
	v_cvt_scalef32_pk_fp8_f32 v138, v148, v149, s36 op_sel:[0,0,0,1]
	v_cvt_scalef32_pk_fp8_f32 v139, v152, v153, s36 op_sel:[0,0,0,1]
	v_cvt_scalef32_pk_fp8_f32 v140, v198, v199, s36 op_sel:[0,0,0,1]
	v_cvt_scalef32_pk_fp8_f32 v141, v220, v221, s36 op_sel:[0,0,0,1]
	s_nop 0
	v_exp_f32_e32 v94, v94
	s_add_i32 s72, s72, s73
	v_mfma_f32_32x32x64_f8f6f4 v[2:17], v[170:177], v[154:161], v[2:17]
	v_exp_f32_e32 v148, v96
	s_add_u32 s72, s72, s81
	v_cvt_scalef32_pk_fp8_f32 v132, v106, v107, s36
	v_exp_f32_e32 v149, v97
	s_or_b32 s79, s72, s77
	v_pk_add_f32 v[96:97], v[136:137], v[82:83]
	v_pk_add_f32 v[106:107], v[134:135], v[84:85]
	v_exp_f32_e32 v66, v66
	v_exp_f32_e32 v67, v67
	v_exp_f32_e32 v68, v68
	v_exp_f32_e32 v69, v69
	v_exp_f32_e32 v95, v95
	v_cvt_scalef32_pk_fp8_f32 v133, v110, v111, s36
	v_pk_add_f32 v[106:107], v[88:89], v[106:107]
	v_pk_add_f32 v[96:97], v[86:87], v[96:97]
	v_exp_f32_e32 v70, v70
	v_exp_f32_e32 v71, v71
	v_exp_f32_e32 v72, v72
	v_exp_f32_e32 v73, v73
	v_cvt_scalef32_pk_fp8_f32 v132, v108, v109, s36 op_sel:[0,0,0,1]
	v_cvt_scalef32_pk_fp8_f32 v133, v112, v113, s36 op_sel:[0,0,0,1]
	v_pk_add_f32 v[96:97], v[90:91], v[96:97]
	v_pk_add_f32 v[106:107], v[92:93], v[106:107]
	v_exp_f32_e32 v74, v74
	v_mfma_f32_32x32x64_f8f6f4 v[34:49], v[162:169], v[184:191], v[34:49]
	v_exp_f32_e32 v75, v75
	v_exp_f32_e32 v76, v76
	v_exp_f32_e32 v77, v77
	v_exp_f32_e32 v78, v78
	v_exp_f32_e32 v79, v79
	s_nop 0
	v_exp_f32_e32 v80, v80
	v_exp_f32_e32 v81, v81
	s_nop 0
	s_nop 0
	v_cvt_scalef32_pk_fp8_f32 v142, v82, v83, s36
	s_nop 0
	v_cvt_scalef32_pk_fp8_f32 v143, v86, v87, s36
	v_cvt_scalef32_pk_fp8_f32 v144, v90, v91, s36
	v_cvt_scalef32_pk_fp8_f32 v142, v84, v85, s36 op_sel:[0,0,0,1]
	v_pk_add_f32 v[82:83], v[150:151], v[66:67]
	v_pk_add_f32 v[84:85], v[146:147], v[68:69]
	s_mulk_i32 s49, 0x2800
	v_pk_add_f32 v[184:185], v[148:149], v[106:107]
	v_pk_add_f32 v[186:187], v[94:95], v[96:97]
	v_cvt_scalef32_pk_fp8_f32 v145, v94, v95, s36
	v_cvt_scalef32_pk_fp8_f32 v143, v88, v89, s36 op_sel:[0,0,0,1]
	v_cvt_scalef32_pk_fp8_f32 v144, v92, v93, s36 op_sel:[0,0,0,1]
	v_mfma_f32_32x32x64_f8f6f4 v[18:33], v[162:169], v[154:161], v[18:33]
	v_add_f32_e64 v84, v72, v84
	v_add_f32_e64 v85, v73, v85
	v_add_f32_e64 v82, v70, v82
	v_add_f32_e64 v83, v71, v83
	s_nop 0
	s_nop 0
	s_nop 0
	s_nop 0
	s_add_i32 s6, s49, 0
	v_add_f32_e64 v82, v74, v82
	v_add_f32_e64 v83, v75, v83
	v_add_f32_e64 v84, v76, v84
	v_add_f32_e64 v85, v77, v85
	v_cvt_scalef32_pk_fp8_f32 v134, v66, v67, s36
	v_cvt_scalef32_pk_fp8_f32 v135, v70, v71, s36
	v_cvt_scalef32_pk_fp8_f32 v136, v74, v75, s36
	v_cvt_scalef32_pk_fp8_f32 v137, v78, v79, s36
	v_pk_add_f32 v[188:189], v[80:81], v[84:85]
	v_pk_add_f32 v[190:191], v[78:79], v[82:83]
	v_add_u32_e32 v106, s6, v216
	v_add_u32_e32 v107, s6, v217
	v_cvt_scalef32_pk_fp8_f32 v145, v148, v149, s36 op_sel:[0,0,0,1]
	v_cvt_scalef32_pk_fp8_f32 v134, v68, v69, s36 op_sel:[0,0,0,1]
	v_cvt_scalef32_pk_fp8_f32 v135, v72, v73, s36 op_sel:[0,0,0,1]
	v_cvt_scalef32_pk_fp8_f32 v136, v76, v77, s36 op_sel:[0,0,0,1]
	v_cvt_scalef32_pk_fp8_f32 v137, v80, v81, s36 op_sel:[0,0,0,1]
	s_waitcnt lgkmcnt(0)
	v_mfma_f32_32x32x64_f8f6f4 v[82:97], v[98:105], v[114:121], 0
	ds_read_b128 v[154:157], v219 offset:5120
	ds_read_b128 v[158:161], v219 offset:5136
	ds_read_b128 v[146:149], v219 offset:7680
	ds_read_b128 v[150:153], v219 offset:7696
	s_cmpk_gt_i32 s42, 0x1ff
	s_cbranch_scc1 .Lmy_rd0_ldum
	s_add_i32 s72, s61, -1
	s_cmp_lt_u32 s72, 20
	s_cbranch_scc0 .Lmy_rd0_noc
	s_waitcnt vmcnt(4)
	v_cvt_scalef32_pk_fp8_f32 v236, v236, v240, s62
	v_cvt_scalef32_pk_fp8_f32 v237, v237, v241, s62
	v_cvt_scalef32_pk_fp8_f32 v238, v238, v242, s62
	v_cvt_scalef32_pk_fp8_f32 v239, v239, v243, s62
	v_cvt_scalef32_pk_fp8_f32 v236, v244, v248, s62 op_sel:[0,0,0,1]
	v_cvt_scalef32_pk_fp8_f32 v237, v245, v249, s62 op_sel:[0,0,0,1]
	v_cvt_scalef32_pk_fp8_f32 v238, v246, v250, s62 op_sel:[0,0,0,1]
	v_cvt_scalef32_pk_fp8_f32 v239, v247, v251, s62 op_sel:[0,0,0,1]
	ds_write_b32 v252, v236
	ds_write_b32 v252, v237 offset:36
	ds_write_b32 v252, v238 offset:72
	ds_write_b32 v252, v239 offset:108
.Lmy_rd0_noc:
	ds_read2_b32 v[244:245], v253 offset1:1
	ds_read2_b32 v[246:247], v253 offset0:2 offset1:3
	s_cmpk_gt_i32 s42, 0x1ff
	s_cbranch_scc1 .Lmy_rd0_sdum
	s_add_i32 s72, s61, -2
	s_cmp_lt_u32 s72, 20
	s_cbranch_scc0 .Lmy_rd0_sdum
	s_andn2_b32 s73, s65, 1
	s_add_u32 s82, s70, s73
	s_addc_u32 s83, s71, 0
	s_bitcmp1_b32 s65, 0
	s_cbranch_scc1 .Lmy_rd0_sdn
	s_waitcnt lgkmcnt(0)
	global_store_dwordx4 v254, v[244:247], s[82:83]
	s_branch .Lmy_rd0_sdone

; DI void attn_unit_a8(unsigned char* lds, const AttnArgs& a) {
;     ...
;         if (hk == 1) { w_cvt(); w_issue(wj + 1 < AT_NWT ? wj + 1 : AT_NWT - 1); }
;         if (hk == 2) w_store(wj);
;         { const int tn = t + 3; gload(tn < a.t1 ? tn : a.t1 - 1, kl, vl); }
.Lmy_rd0_sdone:
	s_cmpk_gt_i32 s42, 0x1ff
	s_cbranch_scc1 .Lmy_rd0_ld0
	s_cmp_lt_u32 s61, 20
	s_cbranch_scc1 .Lmy_rd0_lgo

; DI void attn_unit_a8(unsigned char* lds, const AttnArgs& a) {
;     ...
;     auto w_cvt = [&]() __attribute__((always_inline)) { unsigned char* t8 = lds + AT_WT + wn4 * WPITCH + 4 * wid;
; #pragma unroll
;         for (int j = 0; j < 4; ++j) *(unsigned*)(t8 + j * WPITCH) = pk4_fp8_mul64(wq[0][j], wq[1][j], wq[2][j], wq[3][j]); };
;     const int wcol = tid >> 1, whalf = tid & 1;
;     const unsigned wper_gu = (unsigned)((wcol >> 7) * 256 + (wcol & 96) + invperm32(wcol & 31)) * 1024u + 16u * whalf;
;     const unsigned wper_dn = (unsigned)fwd_lane16(wcol) * 1024u + 16u * whalf;
;     auto w_store = [&](int j) __attribute__((always_inline)) { const float* src; unsigned char* dst; int ld, n0, k0; bool gu; w_decode(j, src, dst, ld, n0, k0, gu);
;         const int nb = n0 >> 8; const unsigned uni = (unsigned)(gu ? (nb & 3) * 512 + (nb >> 2) * 128 : nb * 256) * 1024u + (unsigned)k0;
;         const unsigned off = (gu ? wper_gu : wper_dn) + uni;
;         const unsigned* t = (const unsigned*)(lds + AT_WT + wcol * WPITCH + 16 * whalf);
;         *(u32x4*)(dst + off) = (u32x4){t[0], t[1], t[2], t[3]}; };
;     const bool wrider = a.wl >= 0;
;     if (wrider) w_issue(0);
;     gload(a.t0, kregA, vregA); gload(a.t0 + 1 < a.t1 ? a.t0 + 1 : a.t0, kregB, vregB);
;     lstore(0, kregA, vregA); lstore(1, kregB, vregB);
;     __syncthreads();
;     asm volatile("" : "+v"(qf8));
;     if (a.t0 + 2 < a.t1) gload(a.t0 + 2, kregA, vregA);
;     f32x16 sx0, sx1, sy0, sy1;
;     sx0 = mfma8(kread(lds, 0), qf8, cinit); sx1 = mfma8(kread(lds, 1), qf8, cinit);
;     int slot = 0;
;     auto step = [&](int t, u32x2& kl, u32x2& vl, const u32x2& ks, const u32x2& vs, f32x16& c0, f32x16& c1, f32x16& n0, f32x16& n1, const int hk, const int wj) __attribute__((always_inline)) {
;         const int slot1 = slot == 2 ? 0 : slot + 1, slot2 = slot1 == 2 ? 0 : slot1 + 1;
;         if (hk == 1) { w_cvt(); w_issue(wj + 1 < AT_NWT ? wj + 1 : AT_NWT - 1); }
;         if (hk == 2) w_store(wj);
;         { const int tn = t + 3; gload(tn < a.t1 ? tn : a.t1 - 1, kl, vl); }
;         const unsigned char* Kb = lds + slot * AT_BUFB; const unsigned char* Kn = lds + slot1 * AT_BUFB;
;         const v8i k0 = kread(Kn, 0), k1 = kread(Kn, 1), v0 = vread(Kb, 0), v1 = vread(Kb, 1);
;         n0 = mfma8(k0, qf8, cinit); n1 = mfma8(k1, qf8, cinit);
;         expsum(c0); expsum(c1);
;         const v8i P = pack8(c0, c1);
.LBB0_702:
	s_lshl_b32 s4, s14, 1
	s_waitcnt lgkmcnt(0)
	s_lshr_b32 s12, s14, 3
	s_and_b32 s4, s4, 0x600
	s_and_b32 s12, s12, 0x80
	s_or_b32 s4, s4, s12
	s_and_b64 s[10:11], s[10:11], exec
	s_cselect_b32 s4, s4, s14
	s_and_b32 s10, s24, 3
	s_add_i32 s10, s63, s10
	s_lshl_b32 s10, s10, 5
	s_lshl_b32 s4, s4, 10
	s_add_i32 s15, s4, s10
	s_min_i32 s4, s56, 63
	s_cmp_lt_u32 s56, 60
	s_cselect_b64 s[10:11], -1, 0
	s_lshl_b32 s4, s4, 6
	v_pk_add_f32 v[48:49], v[146:147], v[110:111]
	s_add_i32 s14, s4, 0x100
	s_add_i32 s63, s4, 0xfffff100
	v_pk_add_f32 v[46:47], v[150:151], v[108:109]
	v_pk_add_f32 v[48:49], v[148:149], v[48:49]
	s_and_b64 s[12:13], s[10:11], exec
	v_pk_add_f32 v[46:47], v[142:143], v[46:47]
	v_pk_add_f32 v[48:49], v[58:59], v[48:49]
	s_cselect_b32 s12, s14, s63
	s_add_i32 s25, s25, 1
	v_pk_add_f32 v[46:47], v[144:145], v[46:47]
	v_pk_add_f32 v[48:49], v[60:61], v[48:49]
	s_and_b64 s[6:7], s[6:7], exec
	v_pk_add_f32 v[46:47], v[52:53], v[46:47]
	v_pk_add_f32 v[48:49], v[50:51], v[48:49]
	s_cselect_b32 s14, 0, s25
	v_pk_add_f32 v[46:47], v[56:57], v[46:47]
	v_pk_add_f32 v[48:49], v[54:55], v[48:49]
	s_mul_i32 s6, s14, 0x4680
	v_pk_add_f32 v[38:39], v[38:39], v[46:47]
	v_pk_add_f32 v[36:37], v[36:37], v[48:49]
	v_add_u32_e32 v48, 0xd808, v163
	v_add_u32_e32 v134, s6, v157
	v_pk_add_f32 v[50:51], v[42:43], v[38:39]
	v_pk_add_f32 v[108:109], v[40:41], v[36:37]
	v_add_u32_e32 v45, 0xd800, v163
	ds_read_b128 v[36:39], v134
	ds_read_b128 v[40:43], v134 offset:16
	ds_read2_b32 v[46:47], v45 offset1:1
	ds_read2_b32 v[48:49], v48 offset1:1
	v_pk_add_f32 v[110:111], v[34:35], v[50:51]
	v_add_u32_e32 v34, v44, v158
	v_lshl_or_b32 v34, v34, 10, v160
	v_add_u32_e32 v34, s15, v34
	s_waitcnt lgkmcnt(0)
	global_store_dwordx4 v34, v[46:49], s[8:9]
	v_add_u32_e32 v34, s12, v154
	s_and_b64 s[8:9], s[10:11], exec
	v_ashrrev_i32_e32 v35, 31, v34
	s_cselect_b32 s9, s59, s61
	s_cselect_b32 s8, s58, s60
	v_lshlrev_b64 v[34:35], 7, v[34:35]
	v_mfma_f32_32x32x64_f8f6f4 v[50:65], v[36:43], v[98:105], 0
	v_lshl_add_u64 v[42:43], s[8:9], 0, v[34:35]
	v_lshl_add_u64 v[42:43], v[42:43], 0, v[130:131]
	ds_read_b128 v[34:37], v134 offset:2560
	ds_read_b128 v[38:41], v134 offset:2576
	global_load_dwordx2 v[134:135], v[42:43], off
	v_lshl_add_u64 v[42:43], v[132:133], 0, s[4:5]
	global_load_dwordx2 v[136:137], v[42:43], off offset:256
	v_exp_f32_e32 v82, v82
	v_exp_f32_e32 v83, v83
	v_exp_f32_e32 v86, v86
	v_exp_f32_e32 v87, v87
	v_exp_f32_e32 v90, v90
	v_exp_f32_e32 v91, v91
	v_exp_f32_e32 v94, v94
	v_exp_f32_e32 v95, v95
	v_exp_f32_e32 v150, v66
	v_exp_f32_e32 v151, v67
	v_exp_f32_e32 v174, v70
	v_exp_f32_e32 v175, v71
	v_exp_f32_e32 v74, v74
	v_exp_f32_e32 v75, v75
	v_exp_f32_e32 v78, v78
	v_exp_f32_e32 v79, v79
	ds_read_b128 v[142:145], v164 offset:5120
	ds_read_b128 v[146:149], v164 offset:5136
	ds_read_b128 v[166:169], v164 offset:7680
	ds_read_b128 v[170:173], v164 offset:7696
	v_exp_f32_e32 v84, v84
	v_exp_f32_e32 v85, v85
	v_exp_f32_e32 v88, v88
	v_exp_f32_e32 v89, v89
	v_exp_f32_e32 v92, v92
	v_exp_f32_e32 v93, v93
	v_exp_f32_e32 v96, v96
	v_exp_f32_e32 v97, v97
	v_exp_f32_e32 v164, v68
	v_exp_f32_e32 v165, v69
	v_exp_f32_e32 v176, v72
	v_exp_f32_e32 v177, v73
	v_exp_f32_e32 v76, v76
	v_exp_f32_e32 v77, v77
	v_exp_f32_e32 v80, v80
	v_exp_f32_e32 v81, v81
	s_nop 0
	s_nop 0
	s_nop 0
	s_nop 0
	s_nop 0
	s_nop 0
	s_nop 0
	s_nop 0
	v_cvt_scalef32_pk_fp8_f32 v66, v82, v83, s48
	v_cvt_scalef32_pk_fp8_f32 v70, v150, v151, s48
	v_cvt_scalef32_pk_fp8_f32 v67, v86, v87, s48
	v_cvt_scalef32_pk_fp8_f32 v71, v174, v175, s48
	v_cvt_scalef32_pk_fp8_f32 v68, v90, v91, s48
	v_cvt_scalef32_pk_fp8_f32 v72, v74, v75, s48
	v_cvt_scalef32_pk_fp8_f32 v69, v94, v95, s48
	v_cvt_scalef32_pk_fp8_f32 v73, v78, v79, s48
	v_cvt_scalef32_pk_fp8_f32 v66, v84, v85, s48 op_sel:[0,0,0,1]
	v_cvt_scalef32_pk_fp8_f32 v70, v164, v165, s48 op_sel:[0,0,0,1]
	v_cvt_scalef32_pk_fp8_f32 v67, v88, v89, s48 op_sel:[0,0,0,1]
	v_cvt_scalef32_pk_fp8_f32 v71, v176, v177, s48 op_sel:[0,0,0,1]
	v_cvt_scalef32_pk_fp8_f32 v68, v92, v93, s48 op_sel:[0,0,0,1]
	v_cvt_scalef32_pk_fp8_f32 v72, v76, v77, s48 op_sel:[0,0,0,1]
	v_cvt_scalef32_pk_fp8_f32 v69, v96, v97, s48 op_sel:[0,0,0,1]
	v_cvt_scalef32_pk_fp8_f32 v73, v80, v81, s48 op_sel:[0,0,0,1]
	s_waitcnt lgkmcnt(4)
	v_mfma_f32_32x32x64_f8f6f4 v[34:49], v[34:41], v[98:105], 0
	v_add_f32_e64 v110, v110, v82
	v_add_f32_e64 v111, v111, v83
	v_add_f32_e64 v82, v108, v84
	v_add_f32_e64 v83, v109, v85
	v_add_f32_e64 v84, v86, v110
	v_add_f32_e64 v85, v87, v111
	v_add_f32_e64 v82, v88, v82
	v_add_f32_e64 v83, v89, v83
	s_addk_i32 s6, 0x4680
	v_add_f32_e64 v84, v90, v84
	v_add_f32_e64 v85, v91, v85
	v_add_f32_e64 v82, v92, v82
	v_add_f32_e64 v83, v93, v83
	s_cmp_lg_u32 s14, 2
	v_pk_add_f32 v[82:83], v[96:97], v[82:83]
	v_pk_add_f32 v[84:85], v[94:95], v[84:85]
	s_cselect_b32 s4, s6, 0
	v_pk_add_f32 v[84:85], v[150:151], v[84:85]
	v_pk_add_f32 v[82:83], v[164:165], v[82:83]
	s_add_i32 s4, s4, 0
	v_pk_add_f32 v[82:83], v[176:177], v[82:83]
	s_waitcnt lgkmcnt(2)
	v_mfma_f32_32x32x64_f8f6f4 v[18:33], v[142:149], v[66:73], v[18:33]
	v_add_f32_e64 v84, v174, v84
	v_add_f32_e64 v85, v175, v85
	v_add_f32_e64 v76, v76, v82
	v_add_f32_e64 v77, v77, v83
	v_add_f32_e64 v74, v74, v84
	v_add_f32_e64 v75, v75, v85
	s_add_i32 s24, s24, 1
	s_add_i32 s56, s56, 2
	s_addk_i32 s19, 0x80
	v_add_f32_e64 v110, v80, v76
	v_add_f32_e64 v111, v81, v77
	v_add_f32_e64 v108, v78, v74
	v_add_f32_e64 v109, v79, v75
	s_cmp_lg_u32 s24, 4
	s_waitcnt lgkmcnt(0)
	v_mfma_f32_32x32x64_f8f6f4 v[2:17], v[166:173], v[66:73], v[2:17]
	v_add_u32_e32 v66, s4, v155
	s_waitcnt vmcnt(4)
	ds_write_b64 v66, v[138:139]
	v_add_u32_e32 v66, s4, v156
	v_add_u32_e32 v66, 0x1400, v66
	s_waitcnt vmcnt(3)
	ds_write2_b32 v66, v140, v141 offset1:8
	s_waitcnt lgkmcnt(0)
	s_barrier
	s_cbranch_scc0 .LBB0_712
.LBB0_703:
	s_min_u32 s15, s24, 2
	s_add_i32 s15, s15, 1
	s_lshl_b32 s4, s15, 7
	s_and_b32 s4, s4, 0x1e00
	s_nop 0
	s_nop 0
	s_add_i32 s6, s4, s62
	v_cvt_scalef32_pk_fp8_f32 v66, v116, v112, s47
	v_cvt_scalef32_pk_fp8_f32 v67, v117, v113, s47
	s_mul_hi_u32 s4, s6, 0xaaaaaaab
	v_cvt_scalef32_pk_fp8_f32 v66, v120, v124, s47 op_sel:[0,0,0,1]
	v_cvt_scalef32_pk_fp8_f32 v67, v121, v125, s47 op_sel:[0,0,0,1]
	v_add_u32_e32 v68, 0xd800, v162
	s_lshr_b32 s4, s4, 6
	ds_write2_b32 v68, v66, v67 offset1:9
	s_nop 0
	s_nop 0
	s_mul_i32 s63, s4, 0xffffffa0
	v_cvt_scalef32_pk_fp8_f32 v66, v118, v114, s47
	v_cvt_scalef32_pk_fp8_f32 v67, v119, v115, s47
	s_add_i32 s63, s63, s6
	v_cvt_scalef32_pk_fp8_f32 v66, v122, v126, s47 op_sel:[0,0,0,1]
	v_cvt_scalef32_pk_fp8_f32 v67, v123, v127, s47 op_sel:[0,0,0,1]
	s_mov_b64 s[10:11], s[0:1]
	s_cmp_gt_i32 s63, 63
	s_mov_b64 s[12:13], -1
	ds_write2_b32 v68, v66, v67 offset0:18 offset1:27
	s_cbranch_scc0 .LBB0_705
	s_load_dwordx2 s[6:7], s[10:11], 0xc0
	s_lshl_b64 s[8:9], s[4:5], 22
	s_mov_b64 s[12:13], 0
	s_waitcnt lgkmcnt(0)
	s_add_u32 s6, s6, s8
	s_addc_u32 s7, s7, s9
	s_and_b32 s8, s63, 0x7ffffffc
	s_sub_i32 s25, s8, 64

; DI f32x16 mfma8(v8i a, v8i b, f32x16 c) { return __builtin_amdgcn_mfma_scale_f32_32x32x64_f8f6f4(a, b, c, 0, 0, 0, 0, 0, 0); }
; DI void attn_unit_d8(unsigned char* lds, const AttnArgs& a) {
;     ...
;     auto tile = [&](const unsigned char* Kb, const unsigned char* Kn, v8i& Pa, v8i& Pb, v8i& v0, v8i& v1, const v8i& Qa, const v8i& Qb, const v8i& w0, const v8i& w1) __attribute__((always_inline)) {
;         qk(Kb, 1, s1a, s1b);
;         v0 = rd32(Kb + voff); v1 = rd32(Kb + voff + 32 * A8_PITCH);
;         o0[0] = mfma8(w0, Qa, o0[0]); o1[0] = mfma8(w0, Qb, o1[0]); o0[1] = mfma8(w1, Qa, o0[1]); o1[1] = mfma8(w1, Qb, o1[1]);
;         expsum(s0a, l0); expsum(s0b, l1); pack4(s0a, Pa, 0); pack4(s0b, Pb, 0);
;         qk(Kn, 0, s0a, s0b);
;         expsum(s1a, l0); expsum(s1b, l1); pack4(s1a, Pa, 4); pack4(s1b, Pb, 4);
; #pragma unroll
;         for (int i = 0; i < 8; ++i) { __builtin_amdgcn_sched_group_barrier(0x008, 1, 0); __builtin_amdgcn_sched_group_barrier(0x402, 22, 0); }
;     };
;     for (int t = a.t0; t < a.t1; t += 2) {
;         const int s1 = sb + 1 >= 5 ? sb - 4 : sb + 1, s2 = sb + 2 >= 5 ? sb - 3 : sb + 2, s3 = sb + 3 >= 5 ? sb - 2 : sb + 3, s4 = sb + 4 >= 5 ? sb - 1 : sb + 4;
;         { const int ta = t + 3, tb = t + 4; gload(ta < a.t1 ? ta : a.t1 - 1, kreg0, vreg0); gload(tb < a.t1 ? tb : a.t1 - 1, kreg1, vreg1); }
;         tile(lds + sb * D8_SLOT, lds + s1 * D8_SLOT, PaX, PbX, vX0, vX1, PaY, PbY, vY0, vY1);
.LBB0_1888:
	s_add_i32 s22, s22, 2
	s_mul_i32 s8, s23, 0x2800
	s_cmp_gt_i32 s23, 3
	v_mfma_f32_32x32x64_f8f6f4 v[50:65], v[154:161], v[138:145], v[50:65]
	v_exp_f32_e32 v194, v90
	v_add_u32_e32 v90, s8, v219
	s_cselect_b32 s8, -4, 1
	s_add_i32 s51, s8, s23
	s_cmp_gt_i32 s23, 2
	s_cselect_b32 s8, -3, 2
	s_add_i32 s8, s8, s23
	s_cmp_gt_i32 s23, 1
	s_cselect_b32 s52, -2, 3
	s_add_i32 s52, s52, s23
	s_cmp_gt_i32 s23, 0
	s_cselect_b32 s53, -1, 4
	s_min_u32 s56, s22, 64
	s_add_i32 s53, s53, s23
	s_cmp_lt_u32 s22, 61
	s_mul_i32 s50, s8, 0x2800
	s_mov_b32 s23, s8
	s_cselect_b64 s[54:55], -1, 0
	s_lshl_b32 s8, s56, 6
	s_add_i32 s56, s8, 0xc0
	s_add_i32 s57, s8, 0xfffff0c0
	s_and_b64 s[54:55], s[54:55], exec
	v_lshl_add_u64 v[98:99], v[184:185], 0, s[8:9]
	s_cselect_b32 s8, s56, s57
	s_cselect_b32 s55, s19, s21
	s_cselect_b32 s54, s18, s20
	s_min_u32 s58, s22, 63
	v_exp_f32_e32 v200, v82
	v_exp_f32_e32 v201, v83
	v_exp_f32_e32 v198, v84
	v_exp_f32_e32 v199, v85
	v_exp_f32_e32 v202, v86
	v_exp_f32_e32 v203, v87
	v_exp_f32_e32 v196, v88
	v_exp_f32_e32 v197, v89
	ds_read_b128 v[82:85], v90 offset:2560
	ds_read_b128 v[86:89], v90 offset:2576
	global_load_dwordx2 v[204:205], v[98:99], off offset:192
	v_add_u32_e32 v98, s8, v182
	s_cmp_lt_u32 s22, 60
	v_ashrrev_i32_e32 v99, 31, v98
	s_cselect_b64 s[56:57], -1, 0
	s_lshl_b32 s8, s58, 6
	v_lshlrev_b64 v[98:99], 8, v[98:99]
	s_add_i32 s58, s8, 0x100
	s_add_i32 s59, s8, 0xfffff100
	v_lshl_add_u64 v[98:99], s[54:55], 0, v[98:99]
	s_and_b64 s[54:55], s[56:57], exec
	v_lshl_add_u64 v[100:101], v[184:185], 0, s[8:9]
	s_cselect_b32 s8, s58, s59
	v_lshl_add_u64 v[220:221], v[98:99], 0, v[178:179]
	v_add_u32_e32 v98, s8, v182
	v_ashrrev_i32_e32 v99, 31, v98
	s_cselect_b32 s55, s19, s21
	s_cselect_b32 s54, s18, s20
	v_lshlrev_b64 v[98:99], 8, v[98:99]
	v_lshl_add_u64 v[98:99], s[54:55], 0, v[98:99]
	global_load_dwordx2 v[206:207], v[100:101], off offset:256
	v_lshl_add_u64 v[222:223], v[98:99], 0, v[178:179]
	s_waitcnt lgkmcnt(0)
	v_mfma_f32_32x32x64_f8f6f4 v[98:113], v[82:89], v[114:121], 0
	v_exp_f32_e32 v195, v91
	v_exp_f32_e32 v224, v92
	v_exp_f32_e32 v225, v93
	v_exp_f32_e32 v226, v94
	v_exp_f32_e32 v227, v95
	v_exp_f32_e32 v228, v96
	v_exp_f32_e32 v229, v97
	ds_read_b128 v[170:173], v90 offset:5120
	ds_read_b128 v[174:177], v90 offset:5136
	ds_read_b128 v[162:165], v90 offset:7680
	ds_read_b128 v[166:169], v90 offset:7696
	v_pk_add_f32 v[90:91], v[188:189], v[200:201]
	v_pk_add_f32 v[92:93], v[186:187], v[198:199]
	v_pk_add_f32 v[90:91], v[202:203], v[90:91]
	v_pk_add_f32 v[92:93], v[196:197], v[92:93]
	v_pk_add_f32 v[90:91], v[194:195], v[90:91]
	v_pk_add_f32 v[92:93], v[224:225], v[92:93]
	v_exp_f32_e32 v66, v66
	v_exp_f32_e32 v67, v67
	v_exp_f32_e32 v68, v68
	v_exp_f32_e32 v69, v69
	v_exp_f32_e32 v70, v70
	v_exp_f32_e32 v71, v71
	v_exp_f32_e32 v72, v72
	v_pk_add_f32 v[230:231], v[228:229], v[92:93]
	v_pk_add_f32 v[232:233], v[226:227], v[90:91]
	v_mfma_f32_32x32x64_f8f6f4 v[82:97], v[82:89], v[122:129], 0
	v_exp_f32_e32 v73, v73
	v_exp_f32_e32 v74, v74
	v_exp_f32_e32 v75, v75
	v_exp_f32_e32 v76, v76
	v_exp_f32_e32 v77, v77
	v_exp_f32_e32 v78, v78
	v_exp_f32_e32 v79, v79
	v_exp_f32_e32 v80, v80
	v_exp_f32_e32 v81, v81
	v_pk_add_f32 v[188:189], v[192:193], v[66:67]
	v_pk_add_f32 v[190:191], v[190:191], v[68:69]
	s_nop 0
	v_pk_add_f32 v[188:189], v[70:71], v[188:189]
	v_pk_add_f32 v[190:191], v[72:73], v[190:191]
	s_nop 0
	v_cvt_scalef32_pk_fp8_f32 v186, v200, v201, s36
	v_pk_add_f32 v[188:189], v[74:75], v[188:189]
	v_pk_add_f32 v[190:191], v[76:77], v[190:191]
	v_cvt_scalef32_pk_fp8_f32 v187, v202, v203, s36
	v_cvt_scalef32_pk_fp8_f32 v186, v198, v199, s36 op_sel:[0,0,0,1]
	v_pk_add_f32 v[192:193], v[78:79], v[188:189]
	v_pk_add_f32 v[190:191], v[80:81], v[190:191]
	v_mfma_f32_32x32x64_f8f6f4 v[2:17], v[154:161], v[130:137], v[2:17]
	s_nop 0
	s_nop 0
	s_nop 0
	s_nop 0
	s_nop 0
	s_nop 0
	s_mulk_i32 s51, 0x2800
	v_cvt_scalef32_pk_fp8_f32 v188, v194, v195, s36
	v_cvt_scalef32_pk_fp8_f32 v189, v226, v227, s36
	v_cvt_scalef32_pk_fp8_f32 v154, v66, v67, s36
	v_cvt_scalef32_pk_fp8_f32 v155, v70, v71, s36
	v_cvt_scalef32_pk_fp8_f32 v156, v74, v75, s36
	v_cvt_scalef32_pk_fp8_f32 v157, v78, v79, s36
	v_cvt_scalef32_pk_fp8_f32 v187, v196, v197, s36 op_sel:[0,0,0,1]
	v_add_u32_e32 v234, s51, v219
	v_cvt_scalef32_pk_fp8_f32 v188, v224, v225, s36 op_sel:[0,0,0,1]
	v_cvt_scalef32_pk_fp8_f32 v189, v228, v229, s36 op_sel:[0,0,0,1]
	v_cvt_scalef32_pk_fp8_f32 v154, v68, v69, s36 op_sel:[0,0,0,1]
	v_cvt_scalef32_pk_fp8_f32 v155, v72, v73, s36 op_sel:[0,0,0,1]
	v_cvt_scalef32_pk_fp8_f32 v156, v76, v77, s36 op_sel:[0,0,0,1]
	v_cvt_scalef32_pk_fp8_f32 v157, v80, v81, s36 op_sel:[0,0,0,1]
	v_exp_f32_e32 v98, v98
	v_exp_f32_e32 v99, v99
	v_mfma_f32_32x32x64_f8f6f4 v[34:49], v[146:153], v[138:145], v[34:49]
	v_exp_f32_e32 v100, v100
	v_exp_f32_e32 v101, v101
	v_exp_f32_e32 v102, v102
	v_exp_f32_e32 v103, v103
	v_exp_f32_e32 v104, v104
	v_exp_f32_e32 v105, v105
	v_exp_f32_e32 v106, v106
	v_exp_f32_e32 v107, v107
	v_exp_f32_e32 v108, v108
	v_exp_f32_e32 v109, v109
	v_exp_f32_e32 v110, v110
	v_exp_f32_e32 v111, v111
	v_exp_f32_e32 v112, v112
	v_exp_f32_e32 v113, v113
	ds_read_b128 v[194:197], v234
	ds_read_b128 v[198:201], v234 offset:16
	v_pk_add_f32 v[66:67], v[232:233], v[98:99]
	v_pk_add_f32 v[68:69], v[230:231], v[100:101]
	v_pk_add_f32 v[66:67], v[102:103], v[66:67]
	v_pk_add_f32 v[68:69], v[104:105], v[68:69]
	v_pk_add_f32 v[66:67], v[106:107], v[66:67]
	v_pk_add_f32 v[68:69], v[108:109], v[68:69]
	v_pk_add_f32 v[140:141], v[110:111], v[66:67]
	v_pk_add_f32 v[138:139], v[112:113], v[68:69]
	v_mfma_f32_32x32x64_f8f6f4 v[18:33], v[146:153], v[130:137], v[18:33]
	v_exp_f32_e32 v82, v82
	v_exp_f32_e32 v83, v83
	v_exp_f32_e32 v84, v84
	v_exp_f32_e32 v85, v85
	v_exp_f32_e32 v86, v86
	v_exp_f32_e32 v87, v87
	v_exp_f32_e32 v88, v88
	v_exp_f32_e32 v89, v89
	v_exp_f32_e32 v90, v90
	v_exp_f32_e32 v91, v91
	v_exp_f32_e32 v92, v92
	v_exp_f32_e32 v93, v93
	v_exp_f32_e32 v94, v94
	v_exp_f32_e32 v95, v95
	v_exp_f32_e32 v96, v96
	v_exp_f32_e32 v97, v97
	v_pk_add_f32 v[66:67], v[192:193], v[82:83]
	v_pk_add_f32 v[68:69], v[190:191], v[84:85]
	v_pk_add_f32 v[66:67], v[86:87], v[66:67]
	v_pk_add_f32 v[68:69], v[88:89], v[68:69]
	v_pk_add_f32 v[130:131], v[90:91], v[66:67]
	v_pk_add_f32 v[132:133], v[92:93], v[68:69]
	s_waitcnt lgkmcnt(0)
; DI KParamsPtr kparams() { KParamsPtr p = (KParamsPtr)__builtin_amdgcn_kernarg_segment_ptr(); asm volatile("" : "+s"(p)); return p; }
; DI void attn_unit_a8(unsigned char* lds, const AttnArgs& a) {
;     ...
;     auto w_decode = [&](int j, const float*& src, unsigned char*& dst, int& ld, int& n0, int& k0, bool& gu) __attribute__((always_inline)) {
;         const int g = (j >> 2) * 512 + a.wl, e = g / 96, rr = g - e * 96; KParamsPtr kp = kparams();
;         if (rr < 64) { src = kp->w_gu + ((size_t)a.wli * NE + e) * (1024 * 2048); dst = kp->ws + WS_WGU + (size_t)a.wli * SZ_WGU + (size_t)e * 2048 * 1024; ld = 2048; n0 = (rr & 7) * 256; k0 = ((rr >> 3) * 4 + (j & 3)) * 32; gu = true; }
;         else { const int q = rr - 64; src = kp->w_dn + ((size_t)a.wli * NE + e) * (1024 * 1024); dst = kp->ws + WS_WDN + (size_t)a.wli * SZ_WDN + (size_t)e * 1024 * 1024; ld = 1024; n0 = (q & 3) * 256; k0 = ((q >> 2) * 4 + (j & 3)) * 32; gu = false; } };
;     auto w_issue = [&](int j) __attribute__((always_inline)) { const float* src; unsigned char* dst; int ld, n0, k0; bool gu; w_decode(j, src, dst, ld, n0, k0, gu);
;         const float* p = src + (size_t)(k0 + 4 * wid) * ld + n0 + wn4;
;         wq[0] = __builtin_nontemporal_load((const f32x4*)p); wq[1] = __builtin_nontemporal_load((const f32x4*)(p + ld));
;         wq[2] = __builtin_nontemporal_load((const f32x4*)(p + (size_t)2 * ld)); wq[3] = __builtin_nontemporal_load((const f32x4*)(p + (size_t)3 * ld)); };
; DI void attn_unit_d8(unsigned char* lds, const AttnArgs& a) {
;     ...
;     auto tile = [&](const unsigned char* Kb, const unsigned char* Kn, v8i& Pa, v8i& Pb, v8i& v0, v8i& v1, const v8i& Qa, const v8i& Qb, const v8i& w0, const v8i& w1) __attribute__((always_inline)) {
;         qk(Kb, 1, s1a, s1b);
;         v0 = rd32(Kb + voff); v1 = rd32(Kb + voff + 32 * A8_PITCH);
;         o0[0] = mfma8(w0, Qa, o0[0]); o1[0] = mfma8(w0, Qb, o1[0]); o0[1] = mfma8(w1, Qa, o0[1]); o1[1] = mfma8(w1, Qb, o1[1]);
;         expsum(s0a, l0); expsum(s0b, l1); pack4(s0a, Pa, 0); pack4(s0b, Pb, 0);
;         qk(Kn, 0, s0a, s0b);
;         expsum(s1a, l0); expsum(s1b, l1); pack4(s1a, Pa, 4); pack4(s1b, Pb, 4);
; #pragma unroll
;         for (int i = 0; i < 8; ++i) { __builtin_amdgcn_sched_group_barrier(0x008, 1, 0); __builtin_amdgcn_sched_group_barrier(0x402, 22, 0); }
;     };
	v_mfma_f32_32x32x64_f8f6f4 v[66:81], v[194:201], v[114:121], 0
	s_nop 0
	s_nop 0
	s_nop 0
	s_nop 0
	s_nop 0
	s_nop 0
	s_nop 0
	v_cvt_scalef32_pk_fp8_f32 v190, v98, v99, s36
	v_cvt_scalef32_pk_fp8_f32 v191, v102, v103, s36
	v_cvt_scalef32_pk_fp8_f32 v192, v106, v107, s36
	v_cvt_scalef32_pk_fp8_f32 v193, v110, v111, s36
	v_cvt_scalef32_pk_fp8_f32 v158, v82, v83, s36
	v_cvt_scalef32_pk_fp8_f32 v159, v86, v87, s36
	v_pk_add_f32 v[142:143], v[96:97], v[132:133]
	v_pk_add_f32 v[144:145], v[94:95], v[130:131]
	v_cvt_scalef32_pk_fp8_f32 v160, v90, v91, s36
	v_cvt_scalef32_pk_fp8_f32 v190, v100, v101, s36 op_sel:[0,0,0,1]
	v_cvt_scalef32_pk_fp8_f32 v191, v104, v105, s36 op_sel:[0,0,0,1]
	v_cvt_scalef32_pk_fp8_f32 v192, v108, v109, s36 op_sel:[0,0,0,1]
	v_cvt_scalef32_pk_fp8_f32 v193, v112, v113, s36 op_sel:[0,0,0,1]
	v_cvt_scalef32_pk_fp8_f32 v158, v84, v85, s36 op_sel:[0,0,0,1]
	v_cvt_scalef32_pk_fp8_f32 v159, v88, v89, s36 op_sel:[0,0,0,1]
	v_mfma_f32_32x32x64_f8f6f4 v[98:113], v[194:201], v[122:129], 0
	global_load_dwordx2 v[194:195], v[220:221], off
	global_load_dwordx2 v[196:197], v[222:223], off
	ds_read_b128 v[130:133], v234 offset:2560
	ds_read_b128 v[134:137], v234 offset:2576
	v_exp_f32_e32 v146, v66
	s_lshr_b32 s73, s61, 2
	v_exp_f32_e32 v147, v67
	s_add_i32 s73, s73, 1
	s_mulk_i32 s52, 0x2800
	s_nop 0
	s_add_i32 s8, s52, 0
	v_cvt_scalef32_pk_fp8_f32 v161, v94, v95, s36
	v_add_u32_e32 v224, s8, v183
	v_cvt_scalef32_pk_fp8_f32 v160, v92, v93, s36 op_sel:[0,0,0,1]
	v_cvt_scalef32_pk_fp8_f32 v161, v96, v97, s36 op_sel:[0,0,0,1]
	v_exp_f32_e32 v148, v68
	s_lshl_b32 s73, s73, 9
	v_exp_f32_e32 v149, v69
	s_add_i32 s73, s73, s46
	v_exp_f32_e32 v150, v70
	s_mul_i32 s75, s73, 0xaaab
	v_exp_f32_e32 v151, v71
	s_lshr_b32 s75, s75, 22
	v_exp_f32_e32 v152, v72
	s_mul_i32 s76, s75, 0x60
	v_exp_f32_e32 v153, v73
	s_sub_i32 s76, s73, s76
	v_exp_f32_e32 v198, v74
	s_lshr_b32 s77, s76, 6
	v_exp_f32_e32 v199, v75
	s_lshl_b32 s78, s77, 6
	v_exp_f32_e32 v200, v76
	s_sub_i32 s76, s76, s78
	v_exp_f32_e32 v201, v77
	s_sub_i32 s78, 3, s77
	v_exp_f32_e32 v202, v78
	s_lshr_b32 s79, s76, s78
	v_exp_f32_e32 v203, v79
	s_lshl_b32 s79, s79, 2
	v_exp_f32_e32 v220, v80
	s_and_b32 s81, s61, 3
	v_exp_f32_e32 v221, v81
	s_add_i32 s79, s79, s81
	v_pk_add_f32 v[66:67], v[140:141], v[146:147]
	s_waitcnt lgkmcnt(0)
	v_mfma_f32_32x32x64_f8f6f4 v[82:97], v[130:137], v[114:121], 0
	v_add_f32_e64 v68, v138, v148
	v_add_f32_e64 v69, v139, v149
	v_add_f32_e64 v66, v150, v66
	v_add_f32_e64 v67, v151, v67
	v_add_f32_e64 v68, v152, v68
	v_add_f32_e64 v69, v153, v69
	v_add_f32_e64 v138, v198, v66
	v_add_f32_e64 v139, v199, v67
	v_add_f32_e64 v140, v200, v68
	v_add_f32_e64 v141, v201, v69
	v_exp_f32_e32 v98, v98
	s_lshl_b32 s79, s79, 5
	v_exp_f32_e32 v99, v99
	s_lshl_b32 s81, s63, 2
	v_exp_f32_e32 v100, v100
	s_add_i32 s81, s81, s79
	v_exp_f32_e32 v101, v101
	s_sub_i32 s78, 13, s77
	v_exp_f32_e32 v102, v102
	s_lshl_b32 s81, s81, s78
	v_exp_f32_e32 v103, v103
	s_lshr_b32 s78, 7, s77
	v_exp_f32_e32 v104, v104
	s_and_b32 s78, s76, s78
	v_exp_f32_e32 v105, v105
	s_lshl_b32 s72, s78, 10
	v_exp_f32_e32 v106, v106
	s_add_i32 s81, s81, s72
	v_exp_f32_e32 v107, v107
	s_add_i32 s72, s75, 32
	v_exp_f32_e32 v108, v108
	s_sub_i32 s80, 23, s77
	v_exp_f32_e32 v109, v109
	s_lshl_b32 s72, s72, s80
	v_exp_f32_e32 v110, v110
	s_add_i32 s81, s81, s72
	v_exp_f32_e32 v111, v111
	s_cmp_eq_u32 s77, 0
	s_cselect_b64 s[84:85], s[66:67], s[68:69]
	v_exp_f32_e32 v112, v112
	s_add_u32 s84, s84, s81
	s_addc_u32 s85, s85, 0
	v_exp_f32_e32 v113, v113
	s_lshr_b32 s80, 0x2000, s77
	v_exp_f32_e32 v82, v82
	s_and_b32 s72, s78, 3
	v_mfma_f32_32x32x64_f8f6f4 v[66:81], v[130:137], v[122:129], 0
	v_add_f32_e64 v130, v144, v98
	v_add_f32_e64 v131, v145, v99
	v_add_f32_e64 v132, v142, v100
	v_add_f32_e64 v133, v143, v101
	v_add_f32_e64 v142, v102, v130
	v_add_f32_e64 v143, v103, v131
	v_add_f32_e64 v132, v104, v132
	v_add_f32_e64 v133, v105, v133
	v_add_f32_e64 v134, v220, v140
	v_add_f32_e64 v135, v221, v141
	v_add_f32_e64 v136, v202, v138
	v_add_f32_e64 v137, v203, v139
	s_nop 0
	s_nop 0
	s_nop 0
	s_nop 0
	s_nop 0
	s_nop 0
	v_pk_add_f32 v[142:143], v[106:107], v[142:143]
	v_pk_add_f32 v[132:133], v[108:109], v[132:133]
	v_cvt_scalef32_pk_fp8_f32 v138, v146, v147, s36
	v_cvt_scalef32_pk_fp8_f32 v139, v150, v151, s36
	v_cvt_scalef32_pk_fp8_f32 v140, v198, v199, s36
	v_cvt_scalef32_pk_fp8_f32 v141, v202, v203, s36
	v_cvt_scalef32_pk_fp8_f32 v130, v98, v99, s36
	v_cvt_scalef32_pk_fp8_f32 v131, v102, v103, s36
	v_pk_add_f32 v[146:147], v[112:113], v[132:133]
	v_pk_add_f32 v[150:151], v[110:111], v[142:143]
	v_mfma_f32_32x32x64_f8f6f4 v[50:65], v[170:177], v[186:193], v[50:65]
	v_exp_f32_e32 v83, v83
	s_lshl_b32 s72, s72, 19
	v_exp_f32_e32 v84, v84
	s_lshr_b32 s81, s78, 2
	v_exp_f32_e32 v85, v85
	s_lshl_b32 s81, s81, 17
	v_add_u32_e32 v102, s50, v219
	v_exp_f32_e32 v86, v86
	s_add_i32 s72, s72, s81
	v_exp_f32_e32 v87, v87
	s_lshl_b32 s81, s78, 18
	v_exp_f32_e32 v88, v88
	s_cmp_eq_u32 s77, 0
	s_cselect_b32 s72, s72, s81
; DI unsigned pk4_fp8_mul64(float a, float b, float c, float d) { v2s_t r = {0, 0}; r = __builtin_amdgcn_cvt_scalef32_pk_fp8_f32(r, a, b, 0.015625f, false); r = __builtin_amdgcn_cvt_scalef32_pk_fp8_f32(r, c, d, 0.015625f, true); return __builtin_bit_cast(unsigned, r); }
; DI f32x16 mfma8(v8i a, v8i b, f32x16 c) { return __builtin_amdgcn_mfma_scale_f32_32x32x64_f8f6f4(a, b, c, 0, 0, 0, 0, 0, 0); }
; DI void attn_unit_a8(unsigned char* lds, const AttnArgs& a) {
;     ...
;     auto w_cvt = [&]() __attribute__((always_inline)) { unsigned char* t8 = lds + AT_WT + wn4 * WPITCH + 4 * wid;
; #pragma unroll
;         for (int j = 0; j < 4; ++j) *(unsigned*)(t8 + j * WPITCH) = pk4_fp8_mul64(wq[0][j], wq[1][j], wq[2][j], wq[3][j]); };
;     const int wcol = tid >> 1, whalf = tid & 1;
;     const unsigned wper_gu = (unsigned)((wcol >> 7) * 256 + (wcol & 96) + invperm32(wcol & 31)) * 1024u + 16u * whalf;
;     const unsigned wper_dn = (unsigned)fwd_lane16(wcol) * 1024u + 16u * whalf;
;     auto w_store = [&](int j) __attribute__((always_inline)) { const float* src; unsigned char* dst; int ld, n0, k0; bool gu; w_decode(j, src, dst, ld, n0, k0, gu);
;         const int nb = n0 >> 8; const unsigned uni = (unsigned)(gu ? (nb & 3) * 512 + (nb >> 2) * 128 : nb * 256) * 1024u + (unsigned)k0;
;         const unsigned off = (gu ? wper_gu : wper_dn) + uni;
;         const unsigned* t = (const unsigned*)(lds + AT_WT + wcol * WPITCH + 16 * whalf);
;         *(u32x4*)(dst + off) = (u32x4){t[0], t[1], t[2], t[3]}; };
; DI void attn_unit_d8(unsigned char* lds, const AttnArgs& a) {
;     ...
;     auto tile = [&](const unsigned char* Kb, const unsigned char* Kn, v8i& Pa, v8i& Pb, v8i& v0, v8i& v1, const v8i& Qa, const v8i& Qb, const v8i& w0, const v8i& w1) __attribute__((always_inline)) {
;         qk(Kb, 1, s1a, s1b);
;         v0 = rd32(Kb + voff); v1 = rd32(Kb + voff + 32 * A8_PITCH);
;         o0[0] = mfma8(w0, Qa, o0[0]); o1[0] = mfma8(w0, Qb, o1[0]); o0[1] = mfma8(w1, Qa, o0[1]); o1[1] = mfma8(w1, Qb, o1[1]);
;         expsum(s0a, l0); expsum(s0b, l1); pack4(s0a, Pa, 0); pack4(s0b, Pb, 0);
;         qk(Kn, 0, s0a, s0b);
;         expsum(s1a, l0); expsum(s1b, l1); pack4(s1a, Pa, 4); pack4(s1b, Pb, 4);
; #pragma unroll
;         for (int i = 0; i < 8; ++i) { __builtin_amdgcn_sched_group_barrier(0x008, 1, 0); __builtin_amdgcn_sched_group_barrier(0x402, 22, 0); }
;     };
	v_exp_f32_e32 v89, v89
	s_mul_i32 s81, s77, 0xc000000
	v_cvt_scalef32_pk_fp8_f32 v130, v100, v101, s36 op_sel:[0,0,0,1]
	v_cvt_scalef32_pk_fp8_f32 v131, v104, v105, s36 op_sel:[0,0,0,1]
	v_exp_f32_e32 v90, v90
	s_add_i32 s81, s81, 0x9094000
	v_exp_f32_e32 v91, v91
	s_add_i32 s72, s72, s79
	v_exp_f32_e32 v92, v92
	s_sub_i32 s73, 21, s77
	v_exp_f32_e32 v93, v93
	s_lshl_b32 s73, s75, s73
	ds_read_b128 v[98:101], v102
	ds_read_b128 v[102:105], v102 offset:16
	s_nop 0
	v_cvt_scalef32_pk_fp8_f32 v138, v148, v149, s36 op_sel:[0,0,0,1]
	v_cvt_scalef32_pk_fp8_f32 v139, v152, v153, s36 op_sel:[0,0,0,1]
	v_cvt_scalef32_pk_fp8_f32 v140, v200, v201, s36 op_sel:[0,0,0,1]
	v_cvt_scalef32_pk_fp8_f32 v141, v220, v221, s36 op_sel:[0,0,0,1]
	s_nop 0
	v_exp_f32_e32 v94, v94
	s_add_i32 s72, s72, s73
	v_exp_f32_e32 v95, v95
	s_add_u32 s72, s72, s81
	v_mfma_f32_32x32x64_f8f6f4 v[2:17], v[170:177], v[154:161], v[2:17]
	v_exp_f32_e32 v148, v96
	s_or_b32 s79, s72, s77
	v_cvt_scalef32_pk_fp8_f32 v132, v106, v107, s36
	v_exp_f32_e32 v149, v97
	v_pk_add_f32 v[96:97], v[136:137], v[82:83]
	v_pk_add_f32 v[106:107], v[134:135], v[84:85]
	v_exp_f32_e32 v66, v66
	v_exp_f32_e32 v67, v67
	v_exp_f32_e32 v68, v68
	v_exp_f32_e32 v69, v69
	v_cvt_scalef32_pk_fp8_f32 v133, v110, v111, s36
	v_pk_add_f32 v[106:107], v[88:89], v[106:107]
	v_pk_add_f32 v[96:97], v[86:87], v[96:97]
	v_exp_f32_e32 v70, v70
	v_exp_f32_e32 v71, v71
	v_exp_f32_e32 v72, v72
	v_exp_f32_e32 v73, v73
	v_cvt_scalef32_pk_fp8_f32 v132, v108, v109, s36 op_sel:[0,0,0,1]
	v_cvt_scalef32_pk_fp8_f32 v133, v112, v113, s36 op_sel:[0,0,0,1]
	v_pk_add_f32 v[96:97], v[90:91], v[96:97]
	v_pk_add_f32 v[106:107], v[92:93], v[106:107]
	v_exp_f32_e32 v74, v74
	v_exp_f32_e32 v75, v75
	v_mfma_f32_32x32x64_f8f6f4 v[34:49], v[162:169], v[186:193], v[34:49]
	v_exp_f32_e32 v76, v76
	v_exp_f32_e32 v77, v77
	v_exp_f32_e32 v78, v78
	v_exp_f32_e32 v79, v79
	s_nop 0
	v_exp_f32_e32 v80, v80
	v_exp_f32_e32 v81, v81
	s_nop 0
	s_nop 0
	v_cvt_scalef32_pk_fp8_f32 v142, v82, v83, s36
	s_nop 0
	v_cvt_scalef32_pk_fp8_f32 v143, v86, v87, s36
	v_cvt_scalef32_pk_fp8_f32 v144, v90, v91, s36
	v_cvt_scalef32_pk_fp8_f32 v142, v84, v85, s36 op_sel:[0,0,0,1]
	v_pk_add_f32 v[82:83], v[150:151], v[66:67]
	v_pk_add_f32 v[84:85], v[146:147], v[68:69]
	s_mulk_i32 s53, 0x2800
	v_pk_add_f32 v[186:187], v[148:149], v[106:107]
	v_pk_add_f32 v[188:189], v[94:95], v[96:97]
	v_cvt_scalef32_pk_fp8_f32 v145, v94, v95, s36
	v_cvt_scalef32_pk_fp8_f32 v143, v88, v89, s36 op_sel:[0,0,0,1]
	v_cvt_scalef32_pk_fp8_f32 v144, v92, v93, s36 op_sel:[0,0,0,1]
	v_pk_add_f32 v[84:85], v[72:73], v[84:85]
	v_mfma_f32_32x32x64_f8f6f4 v[18:33], v[162:169], v[154:161], v[18:33]
	v_add_f32_e64 v82, v70, v82
	v_add_f32_e64 v83, v71, v83
	s_nop 0
	s_nop 0
	s_nop 0
	s_nop 0
	s_add_i32 s51, s53, 0
	v_add_f32_e64 v82, v74, v82
	v_add_f32_e64 v83, v75, v83
	v_add_f32_e64 v84, v76, v84
	v_add_f32_e64 v85, v77, v85
	v_cvt_scalef32_pk_fp8_f32 v134, v66, v67, s36
	v_cvt_scalef32_pk_fp8_f32 v135, v70, v71, s36
	v_cvt_scalef32_pk_fp8_f32 v136, v74, v75, s36
	v_cvt_scalef32_pk_fp8_f32 v137, v78, v79, s36
	v_pk_add_f32 v[190:191], v[80:81], v[84:85]
	v_pk_add_f32 v[192:193], v[78:79], v[82:83]
	v_add_u32_e32 v106, s8, v218
	v_add_u32_e32 v107, s51, v183
	v_cvt_scalef32_pk_fp8_f32 v145, v148, v149, s36 op_sel:[0,0,0,1]
	v_cvt_scalef32_pk_fp8_f32 v134, v68, v69, s36 op_sel:[0,0,0,1]
	v_cvt_scalef32_pk_fp8_f32 v135, v72, v73, s36 op_sel:[0,0,0,1]
	v_cvt_scalef32_pk_fp8_f32 v136, v76, v77, s36 op_sel:[0,0,0,1]
	v_cvt_scalef32_pk_fp8_f32 v137, v80, v81, s36 op_sel:[0,0,0,1]
	s_waitcnt lgkmcnt(0)
	v_mfma_f32_32x32x64_f8f6f4 v[82:97], v[98:105], v[114:121], 0
	ds_read_b128 v[154:157], v234 offset:5120
	ds_read_b128 v[158:161], v234 offset:5136
	ds_read_b128 v[146:149], v234 offset:7680
	ds_read_b128 v[150:153], v234 offset:7696
	s_cmpk_gt_i32 s46, 0x1ff
	s_cbranch_scc1 .Lmy_rd1_ldum
	s_add_i32 s72, s61, -1
	s_cmp_lt_u32 s72, 20
	s_cbranch_scc0 .Lmy_rd1_noc
	s_waitcnt vmcnt(4)
	v_cvt_scalef32_pk_fp8_f32 v236, v236, v240, s62
	v_cvt_scalef32_pk_fp8_f32 v237, v237, v241, s62
	v_cvt_scalef32_pk_fp8_f32 v238, v238, v242, s62
	v_cvt_scalef32_pk_fp8_f32 v239, v239, v243, s62
	v_cvt_scalef32_pk_fp8_f32 v236, v244, v248, s62 op_sel:[0,0,0,1]
	v_cvt_scalef32_pk_fp8_f32 v237, v245, v249, s62 op_sel:[0,0,0,1]
	v_cvt_scalef32_pk_fp8_f32 v238, v246, v250, s62 op_sel:[0,0,0,1]
	v_cvt_scalef32_pk_fp8_f32 v239, v247, v251, s62 op_sel:[0,0,0,1]
	ds_write_b32 v252, v236
	ds_write_b32 v252, v237 offset:36
	ds_write_b32 v252, v238 offset:72
	ds_write_b32 v252, v239 offset:108
.Lmy_rd1_noc:
	ds_read2_b32 v[244:245], v253 offset1:1
	ds_read2_b32 v[246:247], v253 offset0:2 offset1:3
	s_cmpk_gt_i32 s46, 0x1ff
	s_cbranch_scc1 .Lmy_rd1_sdum
	s_add_i32 s72, s61, -2
	s_cmp_lt_u32 s72, 20
	s_cbranch_scc0 .Lmy_rd1_sdum
	s_andn2_b32 s73, s65, 1
	s_add_u32 s82, s70, s73
	s_addc_u32 s83, s71, 0
	s_bitcmp1_b32 s65, 0
	s_cbranch_scc1 .Lmy_rd1_sdn
	s_waitcnt lgkmcnt(0)
	global_store_dwordx4 v254, v[244:247], s[82:83]
	s_branch .Lmy_rd1_sdone

; DI void attn_unit_a8(unsigned char* lds, const AttnArgs& a) {
;     ...
;         if (hk == 1) { w_cvt(); w_issue(wj + 1 < AT_NWT ? wj + 1 : AT_NWT - 1); }
;         if (hk == 2) w_store(wj);
;         { const int tn = t + 3; gload(tn < a.t1 ? tn : a.t1 - 1, kl, vl); }
.Lmy_rd1_sdone:
	s_cmpk_gt_i32 s46, 0x1ff
	s_cbranch_scc1 .Lmy_rd1_ld0
	s_cmp_lt_u32 s61, 20
	s_cbranch_scc1 .Lmy_rd1_lgo

; DI void attn_unit_a8(unsigned char* lds, const AttnArgs& a) {
;     ...
;     auto w_cvt = [&]() __attribute__((always_inline)) { unsigned char* t8 = lds + AT_WT + wn4 * WPITCH + 4 * wid;
; #pragma unroll
;         for (int j = 0; j < 4; ++j) *(unsigned*)(t8 + j * WPITCH) = pk4_fp8_mul64(wq[0][j], wq[1][j], wq[2][j], wq[3][j]); };
;     const int wcol = tid >> 1, whalf = tid & 1;
;     const unsigned wper_gu = (unsigned)((wcol >> 7) * 256 + (wcol & 96) + invperm32(wcol & 31)) * 1024u + 16u * whalf;
;     const unsigned wper_dn = (unsigned)fwd_lane16(wcol) * 1024u + 16u * whalf;
;     auto w_store = [&](int j) __attribute__((always_inline)) { const float* src; unsigned char* dst; int ld, n0, k0; bool gu; w_decode(j, src, dst, ld, n0, k0, gu);
;         const int nb = n0 >> 8; const unsigned uni = (unsigned)(gu ? (nb & 3) * 512 + (nb >> 2) * 128 : nb * 256) * 1024u + (unsigned)k0;
;         const unsigned off = (gu ? wper_gu : wper_dn) + uni;
;         const unsigned* t = (const unsigned*)(lds + AT_WT + wcol * WPITCH + 16 * whalf);
;         *(u32x4*)(dst + off) = (u32x4){t[0], t[1], t[2], t[3]}; };
;     const bool wrider = a.wl >= 0;
;     if (wrider) w_issue(0);
;     gload(a.t0, kregA, vregA); gload(a.t0 + 1 < a.t1 ? a.t0 + 1 : a.t0, kregB, vregB);
;     lstore(0, kregA, vregA); lstore(1, kregB, vregB);
;     __syncthreads();
;     asm volatile("" : "+v"(qf8));
;     if (a.t0 + 2 < a.t1) gload(a.t0 + 2, kregA, vregA);
;     f32x16 sx0, sx1, sy0, sy1;
;     sx0 = mfma8(kread(lds, 0), qf8, cinit); sx1 = mfma8(kread(lds, 1), qf8, cinit);
;     int slot = 0;
;     auto step = [&](int t, u32x2& kl, u32x2& vl, const u32x2& ks, const u32x2& vs, f32x16& c0, f32x16& c1, f32x16& n0, f32x16& n1, const int hk, const int wj) __attribute__((always_inline)) {
;         const int slot1 = slot == 2 ? 0 : slot + 1, slot2 = slot1 == 2 ? 0 : slot1 + 1;
;         if (hk == 1) { w_cvt(); w_issue(wj + 1 < AT_NWT ? wj + 1 : AT_NWT - 1); }
;         if (hk == 2) w_store(wj);
;         { const int tn = t + 3; gload(tn < a.t1 ? tn : a.t1 - 1, kl, vl); }
;         const unsigned char* Kb = lds + slot * AT_BUFB; const unsigned char* Kn = lds + slot1 * AT_BUFB;
;         const v8i k0 = kread(Kn, 0), k1 = kread(Kn, 1), v0 = vread(Kb, 0), v1 = vread(Kb, 1);
;         n0 = mfma8(k0, qf8, cinit); n1 = mfma8(k1, qf8, cinit);
;         expsum(c0); expsum(c1);
;         const v8i P = pack8(c0, c1);
.LBB0_1922:
	s_lshl_b32 s8, s18, 1
	s_waitcnt lgkmcnt(0)
	s_lshr_b32 s16, s18, 3
	s_and_b32 s8, s8, 0x600
	s_and_b32 s16, s16, 0x80
	s_or_b32 s8, s8, s16
	s_and_b64 s[14:15], s[14:15], exec
	v_pk_add_f32 v[54:55], v[164:165], v[108:109]
	s_cselect_b32 s8, s8, s18
	s_and_b32 s14, s50, 3
	v_pk_add_f32 v[54:55], v[154:155], v[54:55]
	s_add_i32 s14, s52, s14
	v_pk_add_f32 v[54:55], v[158:159], v[54:55]
	s_lshl_b32 s14, s14, 5
	s_lshl_b32 s8, s8, 10
	v_pk_add_f32 v[56:57], v[160:161], v[110:111]
	v_pk_add_f32 v[46:47], v[46:47], v[54:55]
	s_add_i32 s14, s8, s14
	s_add_i32 s51, s51, 1
	v_pk_add_f32 v[56:57], v[162:163], v[56:57]
	v_pk_add_f32 v[46:47], v[50:51], v[46:47]
	s_and_b64 s[12:13], s[12:13], exec
	v_pk_add_f32 v[56:57], v[152:153], v[56:57]
	v_pk_add_f32 v[40:41], v[40:41], v[46:47]
	s_cselect_b32 s18, 0, s51
	v_pk_add_f32 v[56:57], v[156:157], v[56:57]
	v_pk_add_f32 v[50:51], v[42:43], v[40:41]
	s_mul_i32 s8, s18, 0x4680
	v_pk_add_f32 v[44:45], v[44:45], v[56:57]
	v_add_u32_e32 v58, s8, v169
	v_pk_add_f32 v[110:111], v[34:35], v[50:51]
	v_add_u32_e32 v34, 0xd800, v175
	v_pk_add_f32 v[48:49], v[48:49], v[44:45]
	ds_read_b128 v[40:43], v58
	ds_read_b128 v[44:47], v58 offset:16
	v_add_u32_e32 v35, 0xd808, v175
	ds_read2_b32 v[54:55], v34 offset1:1
	ds_read2_b32 v[56:57], v35 offset1:1
	v_add_u32_e32 v50, v52, v170
	v_lshl_or_b32 v50, v50, 10, v172
	v_add_u32_e32 v50, s14, v50
	v_exp_f32_e32 v82, v82
	s_waitcnt lgkmcnt(0)
	global_store_dwordx4 v50, v[54:57], s[10:11]
	ds_read_b128 v[50:53], v58 offset:2560
	ds_read_b128 v[54:57], v58 offset:2576
	v_add_co_u32_e32 v58, vcc, s70, v148
	v_exp_f32_e32 v83, v83
	s_nop 0
	v_addc_co_u32_e32 v59, vcc, 0, v149, vcc
	global_load_dwordx2 v[136:137], v[58:59], off
	global_load_dwordx2 v[138:139], v[150:151], off offset:256
	v_exp_f32_e32 v86, v86
	v_exp_f32_e32 v87, v87
	v_exp_f32_e32 v90, v90
	v_exp_f32_e32 v91, v91
	v_exp_f32_e32 v94, v94
	v_exp_f32_e32 v95, v95
	v_exp_f32_e32 v164, v66
	v_exp_f32_e32 v165, v67
	v_exp_f32_e32 v178, v70
	v_exp_f32_e32 v179, v71
	v_exp_f32_e32 v74, v74
	v_exp_f32_e32 v75, v75
	v_exp_f32_e32 v78, v78
	v_exp_f32_e32 v79, v79
	ds_read_b128 v[148:151], v176 offset:5120
	ds_read_b128 v[152:155], v176 offset:5136
	ds_read_b128 v[156:159], v176 offset:7680
	ds_read_b128 v[160:163], v176 offset:7696
	v_exp_f32_e32 v84, v84
	v_exp_f32_e32 v85, v85
	v_exp_f32_e32 v88, v88
	v_exp_f32_e32 v89, v89
	v_exp_f32_e32 v92, v92
	v_exp_f32_e32 v93, v93
	v_exp_f32_e32 v96, v96
	v_exp_f32_e32 v97, v97
	v_exp_f32_e32 v176, v68
	v_exp_f32_e32 v177, v69
	v_exp_f32_e32 v180, v72
	v_exp_f32_e32 v181, v73
	v_exp_f32_e32 v76, v76
	v_exp_f32_e32 v77, v77
	v_exp_f32_e32 v80, v80
	v_exp_f32_e32 v81, v81
	s_nop 0
	s_nop 0
	s_nop 0
	s_nop 0
	s_nop 0
	s_nop 0
	s_nop 0
	s_nop 0
	v_cvt_scalef32_pk_fp8_f32 v66, v82, v83, s69
	v_cvt_scalef32_pk_fp8_f32 v70, v164, v165, s69
	v_cvt_scalef32_pk_fp8_f32 v67, v86, v87, s69
	v_cvt_scalef32_pk_fp8_f32 v71, v178, v179, s69
	v_cvt_scalef32_pk_fp8_f32 v68, v90, v91, s69
	v_cvt_scalef32_pk_fp8_f32 v72, v74, v75, s69
	v_cvt_scalef32_pk_fp8_f32 v69, v94, v95, s69
	v_cvt_scalef32_pk_fp8_f32 v73, v78, v79, s69
	v_pk_add_f32 v[36:37], v[36:37], v[48:49]
	v_cvt_scalef32_pk_fp8_f32 v66, v84, v85, s69 op_sel:[0,0,0,1]
	v_cvt_scalef32_pk_fp8_f32 v70, v176, v177, s69 op_sel:[0,0,0,1]
	v_cvt_scalef32_pk_fp8_f32 v67, v88, v89, s69 op_sel:[0,0,0,1]
	v_cvt_scalef32_pk_fp8_f32 v71, v180, v181, s69 op_sel:[0,0,0,1]
	v_cvt_scalef32_pk_fp8_f32 v68, v92, v93, s69 op_sel:[0,0,0,1]
	v_cvt_scalef32_pk_fp8_f32 v72, v76, v77, s69 op_sel:[0,0,0,1]
	v_cvt_scalef32_pk_fp8_f32 v69, v96, v97, s69 op_sel:[0,0,0,1]
	v_cvt_scalef32_pk_fp8_f32 v73, v80, v81, s69 op_sel:[0,0,0,1]
	v_pk_add_f32 v[108:109], v[38:39], v[36:37]
	v_mfma_f32_32x32x64_f8f6f4 v[34:49], v[40:47], v[98:105], 0
	v_add_f32_e64 v110, v110, v82
	v_add_f32_e64 v111, v111, v83
	v_add_f32_e64 v82, v108, v84
	v_add_f32_e64 v83, v109, v85
	v_add_f32_e64 v84, v86, v110
	v_add_f32_e64 v85, v87, v111
	v_add_f32_e64 v82, v88, v82
	v_add_f32_e64 v83, v89, v83
	s_addk_i32 s8, 0x4680
	v_add_f32_e64 v84, v90, v84
	v_add_f32_e64 v85, v91, v85
	v_add_f32_e64 v82, v92, v82
	v_add_f32_e64 v83, v93, v83
	s_cmp_lg_u32 s18, 2
	v_pk_add_f32 v[82:83], v[96:97], v[82:83]
	v_pk_add_f32 v[84:85], v[94:95], v[84:85]
	s_cselect_b32 s8, s8, 0
	v_pk_add_f32 v[84:85], v[164:165], v[84:85]
	v_pk_add_f32 v[82:83], v[176:177], v[82:83]
	s_add_i32 s8, s8, 0
	v_pk_add_f32 v[82:83], v[180:181], v[82:83]
	s_waitcnt lgkmcnt(4)
	v_mfma_f32_32x32x64_f8f6f4 v[50:65], v[50:57], v[98:105], 0
	v_add_f32_e64 v84, v178, v84
	v_add_f32_e64 v85, v179, v85
	v_add_f32_e64 v76, v76, v82
	v_add_f32_e64 v77, v77, v83
	v_add_f32_e64 v74, v74, v84
	v_add_f32_e64 v75, v75, v85
	s_add_i32 s50, s50, 1
	s_addk_i32 s23, 0x80
	v_add_f32_e64 v110, v80, v76
	v_add_f32_e64 v111, v81, v77
	v_add_f32_e64 v108, v78, v74
	v_add_f32_e64 v109, v79, v75
	v_lshl_add_u64 v[140:141], v[140:141], 0, s[36:37]
	s_cmp_lg_u32 s50, 4
	v_lshl_add_u64 v[142:143], v[142:143], 0, s[38:39]
	s_waitcnt lgkmcnt(2)
	v_mfma_f32_32x32x64_f8f6f4 v[18:33], v[148:155], v[66:73], v[18:33]
	s_waitcnt lgkmcnt(0)
	v_mfma_f32_32x32x64_f8f6f4 v[2:17], v[156:163], v[66:73], v[2:17]
	v_add_u32_e32 v66, s8, v131
	s_waitcnt vmcnt(4)
	ds_write_b64 v66, v[144:145]
	v_add_u32_e32 v66, s8, v168
	v_add_u32_e32 v66, 0x1400, v66
	s_waitcnt vmcnt(3)
	ds_write2_b32 v66, v146, v147 offset1:8
	s_waitcnt lgkmcnt(0)
	s_barrier
	s_cbranch_scc0 .LBB0_1931
.LBB0_1923:
	s_min_u32 s19, s50, 2
	s_add_i32 s19, s19, 1
	s_lshl_b32 s8, s19, 7
	s_and_b32 s8, s8, 0x1e00
	s_nop 0
	s_nop 0
	s_add_i32 s10, s8, s76
	v_cvt_scalef32_pk_fp8_f32 v66, v116, v112, s66
	v_cvt_scalef32_pk_fp8_f32 v67, v117, v113, s66
	s_mul_hi_u32 s8, s10, 0xaaaaaaab
	v_cvt_scalef32_pk_fp8_f32 v66, v120, v124, s66 op_sel:[0,0,0,1]
	v_cvt_scalef32_pk_fp8_f32 v67, v121, v125, s66 op_sel:[0,0,0,1]
	v_add_u32_e32 v68, 0xd800, v174
	s_lshr_b32 s8, s8, 6
	ds_write2_b32 v68, v66, v67 offset1:9
	s_nop 0
	s_nop 0
	s_mul_i32 s52, s8, 0xffffffa0
	v_cvt_scalef32_pk_fp8_f32 v66, v118, v114, s66
	v_cvt_scalef32_pk_fp8_f32 v67, v119, v115, s66
	s_add_i32 s52, s52, s10
	v_cvt_scalef32_pk_fp8_f32 v66, v122, v126, s66 op_sel:[0,0,0,1]
	v_cvt_scalef32_pk_fp8_f32 v67, v123, v127, s66 op_sel:[0,0,0,1]
	s_mov_b64 s[14:15], s[0:1]
	s_cmp_gt_i32 s52, 63
	s_mov_b64 s[16:17], -1
	ds_write2_b32 v68, v66, v67 offset0:18 offset1:27
	s_cbranch_scc0 .LBB0_1925
	s_load_dwordx2 s[10:11], s[14:15], 0xc0
	s_lshl_b64 s[12:13], s[8:9], 22
	s_mov_b64 s[16:17], 0
	s_waitcnt lgkmcnt(0)
	s_add_u32 s10, s10, s12
	s_addc_u32 s11, s11, s13
	s_add_u32 s10, s10, 0x8000000
	s_addc_u32 s11, s11, 0
	s_and_b32 s12, s52, 0x7ffffffc
	s_sub_i32 s51, s12, 64
